# prologue queue: strip units fetch the next queue index before their store loop (atomic round trip overlaps the stores)
# speedup vs baseline: 1.0002x; 1.0002x over previous
.LBB0_5:
	s_or_b64 exec, exec, s[4:5]
	s_add_u32 s16, s14, 0x4060
	s_addc_u32 s17, s15, 0
	s_add_u32 s2, s14, 0x1d52ce00
	s_addc_u32 s3, s15, 0
	v_writelane_b32 v252, s2, 11
	s_load_dwordx16 s[36:51], s[0:1], 0x0
	v_mov_b32_e32 v11, 0
	v_writelane_b32 v252, s3, 12
	s_add_u32 s2, s14, 0x1c52ce00
	s_addc_u32 s3, s15, 0
	v_writelane_b32 v252, s2, 13
	v_mov_b32_e32 v1, 0x38d1b717
	v_mov_b32_e32 v78, 0x3c0881c4
	v_writelane_b32 v252, s3, 14
	s_add_u32 s2, s14, 0x1ac2ce00
	s_addc_u32 s3, s15, 0
	v_writelane_b32 v252, s2, 15
	v_mov_b32_e32 v79, 0xbab64f3b
	v_mov_b32_e32 v80, 0xc2f0cb68
	v_writelane_b32 v252, s3, 16
	s_add_u32 s2, s14, 0x79100
	v_writelane_b32 v252, s2, 17
	s_addc_u32 s2, s15, 0
	v_writelane_b32 v252, s2, 18
	s_add_u32 s2, s14, 0xa42ce00
	v_writelane_b32 v252, s2, 19
	s_addc_u32 s2, s15, 0
	v_writelane_b32 v252, s2, 20
	s_add_u32 s2, s14, 0x1d98ce00
	s_addc_u32 s3, s15, 0
	v_writelane_b32 v252, s2, 21
	v_mov_b32_e32 v82, 0x80000
	v_mov_b32_e32 v83, 0x150000
	v_writelane_b32 v252, s3, 22
	s_add_u32 s2, s14, 0x4100
	v_writelane_b32 v252, s2, 23
	s_addc_u32 s2, s15, 0
	v_writelane_b32 v252, s2, 24
	s_add_u32 s2, s14, 0x1542ce00
	v_writelane_b32 v252, s2, 25
	s_addc_u32 s2, s15, 0
	v_writelane_b32 v252, s2, 26
	s_add_u32 s2, s14, 0x1ef8ce00
	s_addc_u32 s3, s15, 0
	v_writelane_b32 v252, s2, 27
	v_mov_b32_e32 v84, 0x700
	v_mov_b32_e32 v85, 0x200
	v_writelane_b32 v252, s3, 28
	s_add_u32 s2, s14, 0xd9d00
	s_addc_u32 s3, s15, 0
	v_writelane_b32 v252, s2, 29
	v_mov_b32_e32 v86, 0x230000
	v_mov_b32_e32 v87, 6
	v_writelane_b32 v252, s3, 30
	s_add_u32 s2, s14, 0x27c8ce00
	v_writelane_b32 v252, s2, 31
	s_addc_u32 s2, s15, 0
	v_writelane_b32 v252, s2, 32
	s_add_u32 s2, s14, 0x27d8ce00
	v_writelane_b32 v252, s2, 33
	s_addc_u32 s2, s15, 0
	v_writelane_b32 v252, s2, 34
	s_add_u32 s2, s14, 0x1fa8ce00
	v_writelane_b32 v252, s2, 35
	s_addc_u32 s2, s15, 0
	v_writelane_b32 v252, s2, 36
	s_add_u32 s2, s14, 0x27a8ce00
	s_addc_u32 s3, s15, 0
	s_waitcnt lgkmcnt(0)
	s_add_u32 s18, s48, 0x60000
	s_addc_u32 s19, s49, 0
	s_load_dwordx16 s[36:51], s[0:1], 0x80
	v_writelane_b32 v252, s2, 37
	v_mov_b32_e32 v88, 0x6000000
	v_not_b32_e32 v89, 63
	v_writelane_b32 v252, s3, 38
	s_waitcnt lgkmcnt(0)
	s_add_u32 s2, s42, 0x110
	s_addc_u32 s3, s43, 0
	s_add_i32 s33, 0, 0x23fd0
	v_mov_b32_e32 v81, s33
	v_not_b32_e32 v90, 31
	v_mov_b32_e32 v91, 0xffc00000
	v_mov_b32_e32 v92, 0x7fc00000
	v_mov_b32_e32 v93, 0x7f800000
	s_movk_i32 s58, 0xdff
	s_movk_i32 s59, 0x13ff
	s_movk_i32 s60, 0x6000
	s_mov_b32 s61, 0xc000
	s_mov_b32 s62, 0x12000
	s_mov_b32 s63, 0x42fe0000
	s_movk_i32 s64, 0x2040
	s_mov_b32 s65, 0x40c0c00
	s_movk_i32 s66, 0x1000
	s_mov_b32 s67, 0x10000
	s_add_i32 s68, 0, 0x16100
	s_movk_i32 s69, 0x1600
	s_mov_b32 s70, 0x18000
	s_mov_b32 s71, 0x24000
	s_mov_b32 s72, 0x30000
	s_mov_b32 s73, 0x3c000
	s_mov_b32 s74, 0x437f0000
	s_brev_b32 s75, 18
	s_mov_b32 s76, 0xfe5163ab
	s_mov_b32 s77, 0x3c439041
	s_mov_b32 s78, 0xdb629599
	s_mov_b32 s79, 0xf534ddc0
	s_mov_b32 s80, 0xfc2757d1
	s_mov_b32 s81, 0x4e441529
	s_mov_b32 s82, 0xa2f9836e
	s_mov_b32 s83, 0x3fc90fda
	s_mov_b32 s84, 0x3f22f983
	s_mov_b32 s85, 0xbfc90fda
	s_brev_b32 s86, 1
	s_mov_b32 s87, 0x7f800000
	s_movk_i32 s88, 0x2100
	s_movk_i32 s89, 0x110
	s_add_i32 s90, 0, 0x2400
	s_movk_i32 s91, 0x1f8
	s_add_i32 s92, 0, 0x6800
	s_add_i32 s93, 0, 0xac00
	s_mov_b32 s94, 0xbb800000
	s_mov_b32 s95, 0x3fb8aa3b
	s_mov_b32 s96, 0xc2ce8ed0
	s_mov_b32 s97, 0x42b17218
	s_mov_b32 s57, 0x467ffc00
	s_mov_b32 s22, 0xb8800000
	s_mov_b32 s21, 0
	v_mov_b32_e32 v200, -1
	s_branch .LBB0_8

.LBB0_8:
	s_waitcnt lgkmcnt(0)
	s_barrier
	v_mov_b32_e32 v2, v0
	s_nop 0
	v_cmp_eq_u32_e32 vcc, 0, v2
	s_and_saveexec_b64 s[4:5], vcc
	s_cbranch_execz .LBB0_12
	s_waitcnt vmcnt(0)
	v_readfirstlane_b32 s6, v200
	s_cmp_lg_u32 s6, -1
	s_cbranch_scc1 .Lqpf_have
	v_mov_b32_e32 v200, 1
	s_nop 0
	global_atomic_add v200, v11, v200, s[16:17] sc0
	s_waitcnt vmcnt(0)
.Lqpf_have:
	v_mov_b32_e32 v3, s33
	s_nop 0
	ds_write_b32 v3, v200
	s_nop 1
	v_mov_b32_e32 v200, -1

.LBB0_220:
	s_or_b64 exec, exec, s[4:5]
	s_nop 0
	v_max_f32_e32 v2, v2, v2
	v_max_f32_e32 v2, 0xda24260, v2
	v_div_scale_f32 v6, s[4:5], v2, v2, s63
	v_rcp_f32_e32 v7, v6
	v_div_scale_f32 v76, vcc, s63, v2, s63
	v_max_f32_e32 v3, v3, v3
	v_fma_f32 v77, -v6, v7, 1.0
	v_fmac_f32_e32 v7, v77, v7
	v_mul_f32_e32 v77, v76, v7
	v_fma_f32 v94, -v6, v77, v76
	v_fmac_f32_e32 v77, v94, v7
	v_max_f32_e32 v3, 0xda24260, v3
	v_fma_f32 v6, -v6, v77, v76
	v_div_scale_f32 v76, s[4:5], v3, v3, s63
	v_rcp_f32_e32 v94, v76
	v_div_fmas_f32 v6, v6, v7, v77
	v_div_fixup_f32 v6, v6, v2, s63
	v_max_f32_e32 v4, v4, v4
	v_fma_f32 v2, -v76, v94, 1.0
	v_fmac_f32_e32 v94, v2, v94
	v_div_scale_f32 v2, vcc, s63, v3, s63
	v_mul_f32_e32 v7, v2, v94
	v_fma_f32 v77, -v76, v7, v2
	v_fmac_f32_e32 v7, v77, v94
	v_fma_f32 v2, -v76, v7, v2
	v_max_f32_e32 v76, 0xda24260, v4
	v_div_scale_f32 v77, s[4:5], v76, v76, s63
	v_rcp_f32_e32 v95, v77
	v_div_fmas_f32 v2, v2, v94, v7
	v_div_fixup_f32 v4, v2, v3, s63
	v_max_f32_e32 v5, v5, v5
	v_fma_f32 v2, -v77, v95, 1.0
	v_fmac_f32_e32 v95, v2, v95
	v_div_scale_f32 v2, vcc, s63, v76, s63
	v_mul_f32_e32 v3, v2, v95
	v_fma_f32 v7, -v77, v3, v2
	v_max_f32_e32 v5, 0xda24260, v5
	v_fmac_f32_e32 v3, v7, v95
	v_div_scale_f32 v7, s[4:5], v5, v5, s63
	v_fma_f32 v2, -v77, v3, v2
	v_rcp_f32_e32 v77, v7
	v_div_fmas_f32 v2, v2, v95, v3
	v_div_fixup_f32 v3, v2, v76, s63
	v_fma_f32 v2, -v7, v77, 1.0
	v_fmac_f32_e32 v77, v2, v77
	v_div_scale_f32 v2, vcc, s63, v5, s63
	v_mul_f32_e32 v76, v2, v77
	v_fma_f32 v94, -v7, v76, v2
	v_fmac_f32_e32 v76, v94, v77
	v_fma_f32 v2, -v7, v76, v2
	v_div_fmas_f32 v2, v2, v77, v76
	v_div_fixup_f32 v2, v2, v5, s63
	v_mul_lo_u32 v5, v22, s64
	v_lshlrev_b32_e32 v22, 16, v73
	v_add3_u32 v5, 0, v5, v59
	v_lshlrev_b32_e32 v7, 16, v72
	v_mul_f32_e32 v22, v6, v22
	v_lshlrev_b32_e32 v59, 16, v74
	v_lshlrev_b32_e32 v76, 16, v75
	v_mul_f32_e32 v7, v6, v7
	v_rndne_f32_e32 v22, v22
	v_mul_f32_e32 v59, v6, v59
	v_mul_f32_e32 v76, v6, v76
	v_rndne_f32_e32 v7, v7
	v_cvt_i32_f32_e32 v22, v22
	v_rndne_f32_e32 v59, v59
	v_rndne_f32_e32 v76, v76
	v_cvt_i32_f32_e32 v7, v7
	v_cvt_i32_f32_sdwa v59, v59 dst_sel:WORD_1 dst_unused:UNUSED_PAD src0_sel:DWORD
	v_cvt_i32_f32_e32 v76, v76
	v_lshlrev_b32_e32 v22, 8, v22
	v_and_b32_e32 v22, 0xff00, v22
	v_and_b32_e32 v59, 0xff0000, v59
	v_perm_b32 v7, v76, v7, s65
	v_or3_b32 v7, v7, v22, v59
	v_and_b32_e32 v59, 0xffff0000, v73
	v_and_b32_e32 v22, 0xffff0000, v72
	v_mul_f32_e32 v59, v4, v59
	v_and_b32_e32 v72, 0xffff0000, v74
	v_and_b32_e32 v73, 0xffff0000, v75
	v_mul_f32_e32 v22, v4, v22
	v_rndne_f32_e32 v59, v59
	v_mul_f32_e32 v72, v4, v72
	v_mul_f32_e32 v73, v4, v73
	v_rndne_f32_e32 v22, v22
	v_cvt_i32_f32_e32 v59, v59
	v_rndne_f32_e32 v72, v72
	v_rndne_f32_e32 v73, v73
	v_cvt_i32_f32_e32 v22, v22
	v_cvt_i32_f32_sdwa v72, v72 dst_sel:WORD_1 dst_unused:UNUSED_PAD src0_sel:DWORD
	v_cvt_i32_f32_e32 v73, v73
	v_lshlrev_b32_e32 v59, 8, v59
	v_and_b32_e32 v59, 0xff00, v59
	v_and_b32_e32 v72, 0xff0000, v72
	v_perm_b32 v22, v73, v22, s65
	v_or3_b32 v22, v22, v59, v72
	v_lshlrev_b32_e32 v72, 16, v69
	v_and_b32_e32 v69, 0xffff0000, v69
	v_lshlrev_b32_e32 v59, 16, v68
	v_lshlrev_b32_e32 v73, 16, v70
	v_lshlrev_b32_e32 v74, 16, v71
	v_and_b32_e32 v68, 0xffff0000, v68
	v_mul_f32_e32 v69, v2, v69
	v_and_b32_e32 v70, 0xffff0000, v70
	v_and_b32_e32 v71, 0xffff0000, v71
	v_mul_f32_e32 v72, v3, v72
	v_mul_f32_e32 v68, v2, v68
	v_rndne_f32_e32 v69, v69
	v_mul_f32_e32 v70, v2, v70
	v_mul_f32_e32 v71, v2, v71
	v_mul_f32_e32 v59, v3, v59
	v_rndne_f32_e32 v72, v72
	v_mul_f32_e32 v73, v3, v73
	v_mul_f32_e32 v74, v3, v74
	v_rndne_f32_e32 v68, v68
	v_cvt_i32_f32_e32 v69, v69
	v_rndne_f32_e32 v70, v70
	v_rndne_f32_e32 v71, v71
	v_rndne_f32_e32 v59, v59
	v_cvt_i32_f32_e32 v72, v72
	v_rndne_f32_e32 v73, v73
	v_rndne_f32_e32 v74, v74
	v_cvt_i32_f32_e32 v68, v68
	v_cvt_i32_f32_sdwa v70, v70 dst_sel:WORD_1 dst_unused:UNUSED_PAD src0_sel:DWORD
	v_cvt_i32_f32_e32 v71, v71
	v_cvt_i32_f32_e32 v59, v59
	v_cvt_i32_f32_sdwa v73, v73 dst_sel:WORD_1 dst_unused:UNUSED_PAD src0_sel:DWORD
	v_cvt_i32_f32_e32 v74, v74
	v_lshlrev_b32_e32 v69, 8, v69
	v_lshlrev_b32_e32 v72, 8, v72
	v_and_b32_e32 v69, 0xff00, v69
	v_and_b32_e32 v70, 0xff0000, v70
	v_perm_b32 v68, v71, v68, s65
	v_and_b32_e32 v72, 0xff00, v72
	v_and_b32_e32 v73, 0xff0000, v73
	v_perm_b32 v59, v74, v59, s65
	v_or3_b32 v68, v68, v69, v70
	v_lshlrev_b32_e32 v70, 16, v65
	v_or3_b32 v59, v59, v72, v73
	v_lshlrev_b32_e32 v69, 16, v64
	v_mul_f32_e32 v70, v6, v70
	v_lshlrev_b32_e32 v71, 16, v66
	v_lshlrev_b32_e32 v72, 16, v67
	v_mul_f32_e32 v69, v6, v69
	v_rndne_f32_e32 v70, v70
	v_mul_f32_e32 v71, v6, v71
	v_mul_f32_e32 v72, v6, v72
	v_rndne_f32_e32 v69, v69
	v_cvt_i32_f32_e32 v70, v70
	v_rndne_f32_e32 v71, v71
	v_rndne_f32_e32 v72, v72
	v_cvt_i32_f32_e32 v69, v69
	v_cvt_i32_f32_sdwa v71, v71 dst_sel:WORD_1 dst_unused:UNUSED_PAD src0_sel:DWORD
	v_cvt_i32_f32_e32 v72, v72
	v_lshlrev_b32_e32 v70, 8, v70
	v_and_b32_e32 v70, 0xff00, v70
	v_and_b32_e32 v71, 0xff0000, v71
	v_perm_b32 v69, v72, v69, s65
	v_or3_b32 v69, v69, v70, v71
	ds_write2st64_b32 v5, v7, v69 offset1:1
	v_and_b32_e32 v7, 0xffff0000, v64
	v_and_b32_e32 v64, 0xffff0000, v65
	v_mul_f32_e32 v64, v4, v64
	v_and_b32_e32 v65, 0xffff0000, v66
	v_and_b32_e32 v66, 0xffff0000, v67
	v_mul_f32_e32 v7, v4, v7
	v_rndne_f32_e32 v64, v64
	v_mul_f32_e32 v65, v4, v65
	v_mul_f32_e32 v66, v4, v66
	v_rndne_f32_e32 v7, v7
	v_cvt_i32_f32_e32 v64, v64
	v_rndne_f32_e32 v65, v65
	v_rndne_f32_e32 v66, v66
	v_cvt_i32_f32_e32 v7, v7
	v_cvt_i32_f32_sdwa v65, v65 dst_sel:WORD_1 dst_unused:UNUSED_PAD src0_sel:DWORD
	v_cvt_i32_f32_e32 v66, v66
	v_lshlrev_b32_e32 v64, 8, v64
	v_and_b32_e32 v64, 0xff00, v64
	v_and_b32_e32 v65, 0xff0000, v65
	v_perm_b32 v7, v66, v7, s65
	v_or3_b32 v64, v7, v64, v65
	v_add_u32_e32 v7, 16, v5
	ds_write2st64_b32 v7, v22, v64 offset0:8 offset1:9
	v_lshlrev_b32_e32 v64, 16, v56
	v_and_b32_e32 v56, 0xffff0000, v56
	v_lshlrev_b32_e32 v22, 16, v55
	v_mul_f32_e32 v64, v3, v64
	v_lshlrev_b32_e32 v65, 16, v57
	v_lshlrev_b32_e32 v66, 16, v58
	v_and_b32_e32 v55, 0xffff0000, v55
	v_mul_f32_e32 v56, v2, v56
	v_and_b32_e32 v57, 0xffff0000, v57
	v_and_b32_e32 v58, 0xffff0000, v58
	v_mul_f32_e32 v22, v3, v22
	v_rndne_f32_e32 v64, v64
	v_mul_f32_e32 v65, v3, v65
	v_mul_f32_e32 v66, v3, v66
	v_mul_f32_e32 v55, v2, v55
	v_rndne_f32_e32 v56, v56
	v_mul_f32_e32 v57, v2, v57
	v_mul_f32_e32 v58, v2, v58
	v_rndne_f32_e32 v22, v22
	v_cvt_i32_f32_e32 v64, v64
	v_rndne_f32_e32 v65, v65
	v_rndne_f32_e32 v66, v66
	v_rndne_f32_e32 v55, v55
	v_cvt_i32_f32_e32 v56, v56
	v_rndne_f32_e32 v57, v57
	v_rndne_f32_e32 v58, v58
	v_cvt_i32_f32_e32 v22, v22
	v_cvt_i32_f32_sdwa v65, v65 dst_sel:WORD_1 dst_unused:UNUSED_PAD src0_sel:DWORD
	v_cvt_i32_f32_e32 v66, v66
	v_cvt_i32_f32_e32 v55, v55
	v_cvt_i32_f32_sdwa v57, v57 dst_sel:WORD_1 dst_unused:UNUSED_PAD src0_sel:DWORD
	v_cvt_i32_f32_e32 v58, v58
	v_lshlrev_b32_e32 v64, 8, v64
	v_lshlrev_b32_e32 v56, 8, v56
	v_and_b32_e32 v64, 0xff00, v64
	v_and_b32_e32 v65, 0xff0000, v65
	v_perm_b32 v22, v66, v22, s65
	v_and_b32_e32 v56, 0xff00, v56
	v_and_b32_e32 v57, 0xff0000, v57
	v_perm_b32 v55, v58, v55, s65
	v_or3_b32 v64, v22, v64, v65
	v_add_u32_e32 v22, 32, v5
	v_or3_b32 v56, v55, v56, v57
	v_add_u32_e32 v55, 48, v5
	v_lshlrev_b32_e32 v57, 16, v61
	ds_write2st64_b32 v22, v59, v64 offset0:16 offset1:17
	ds_write2st64_b32 v55, v68, v56 offset0:24 offset1:25
	v_lshlrev_b32_e32 v56, 16, v60
	v_mul_f32_e32 v57, v6, v57
	v_lshlrev_b32_e32 v58, 16, v62
	v_lshlrev_b32_e32 v59, 16, v63
	v_mul_f32_e32 v56, v6, v56
	v_rndne_f32_e32 v57, v57
	v_mul_f32_e32 v58, v6, v58
	v_mul_f32_e32 v59, v6, v59
	v_rndne_f32_e32 v56, v56
	v_cvt_i32_f32_e32 v57, v57
	v_rndne_f32_e32 v58, v58
	v_rndne_f32_e32 v59, v59
	v_cvt_i32_f32_e32 v56, v56
	v_cvt_i32_f32_sdwa v58, v58 dst_sel:WORD_1 dst_unused:UNUSED_PAD src0_sel:DWORD
	v_cvt_i32_f32_e32 v59, v59
	v_lshlrev_b32_e32 v57, 8, v57
	v_and_b32_e32 v57, 0xff00, v57
	v_and_b32_e32 v58, 0xff0000, v58
	v_perm_b32 v56, v59, v56, s65
	v_or3_b32 v56, v56, v57, v58
	v_and_b32_e32 v58, 0xffff0000, v61
	v_and_b32_e32 v57, 0xffff0000, v60
	v_mul_f32_e32 v58, v4, v58
	v_and_b32_e32 v59, 0xffff0000, v62
	v_and_b32_e32 v60, 0xffff0000, v63
	v_mul_f32_e32 v57, v4, v57
	v_rndne_f32_e32 v58, v58
	v_mul_f32_e32 v59, v4, v59
	v_mul_f32_e32 v60, v4, v60
	v_rndne_f32_e32 v57, v57
	v_cvt_i32_f32_e32 v58, v58
	v_rndne_f32_e32 v59, v59
	v_rndne_f32_e32 v60, v60
	v_cvt_i32_f32_e32 v57, v57
	v_cvt_i32_f32_sdwa v59, v59 dst_sel:WORD_1 dst_unused:UNUSED_PAD src0_sel:DWORD
	v_cvt_i32_f32_e32 v60, v60
	v_lshlrev_b32_e32 v58, 8, v58
	v_and_b32_e32 v58, 0xff00, v58
	v_and_b32_e32 v59, 0xff0000, v59
	v_perm_b32 v57, v60, v57, s65
	v_or3_b32 v57, v57, v58, v59
	v_lshlrev_b32_e32 v59, 16, v52
	v_and_b32_e32 v52, 0xffff0000, v52
	v_lshlrev_b32_e32 v58, 16, v51
	v_lshlrev_b32_e32 v60, 16, v53
	v_lshlrev_b32_e32 v61, 16, v54
	v_and_b32_e32 v51, 0xffff0000, v51
	v_mul_f32_e32 v52, v2, v52
	v_and_b32_e32 v53, 0xffff0000, v53
	v_and_b32_e32 v54, 0xffff0000, v54
	v_mul_f32_e32 v59, v3, v59
	v_mul_f32_e32 v51, v2, v51
	v_rndne_f32_e32 v52, v52
	v_mul_f32_e32 v53, v2, v53
	v_mul_f32_e32 v54, v2, v54
	v_mul_f32_e32 v58, v3, v58
	v_rndne_f32_e32 v59, v59
	v_mul_f32_e32 v60, v3, v60
	v_mul_f32_e32 v61, v3, v61
	v_rndne_f32_e32 v51, v51
	v_cvt_i32_f32_e32 v52, v52
	v_rndne_f32_e32 v53, v53
	v_rndne_f32_e32 v54, v54
	v_rndne_f32_e32 v58, v58
	v_cvt_i32_f32_e32 v59, v59
	v_rndne_f32_e32 v60, v60
	v_rndne_f32_e32 v61, v61
	v_cvt_i32_f32_e32 v51, v51
	v_cvt_i32_f32_sdwa v53, v53 dst_sel:WORD_1 dst_unused:UNUSED_PAD src0_sel:DWORD
	v_cvt_i32_f32_e32 v54, v54
	v_cvt_i32_f32_e32 v58, v58
	v_cvt_i32_f32_sdwa v60, v60 dst_sel:WORD_1 dst_unused:UNUSED_PAD src0_sel:DWORD
	v_cvt_i32_f32_e32 v61, v61
	v_lshlrev_b32_e32 v52, 8, v52
	v_lshlrev_b32_e32 v59, 8, v59
	v_and_b32_e32 v52, 0xff00, v52
	v_and_b32_e32 v53, 0xff0000, v53
	v_perm_b32 v51, v54, v51, s65
	v_and_b32_e32 v59, 0xff00, v59
	v_and_b32_e32 v60, 0xff0000, v60
	v_perm_b32 v58, v61, v58, s65
	v_or3_b32 v51, v51, v52, v53
	v_lshlrev_b32_e32 v53, 16, v48
	v_and_b32_e32 v48, 0xffff0000, v48
	v_or3_b32 v58, v58, v59, v60
	v_lshlrev_b32_e32 v52, 16, v47
	v_lshlrev_b32_e32 v54, 16, v49
	v_lshlrev_b32_e32 v59, 16, v50
	v_and_b32_e32 v47, 0xffff0000, v47
	v_mul_f32_e32 v48, v4, v48
	v_and_b32_e32 v49, 0xffff0000, v49
	v_and_b32_e32 v50, 0xffff0000, v50
	v_mul_f32_e32 v47, v4, v47
	v_rndne_f32_e32 v48, v48
	v_mul_f32_e32 v49, v4, v49
	v_mul_f32_e32 v50, v4, v50
	v_rndne_f32_e32 v47, v47
	v_cvt_i32_f32_e32 v48, v48
	v_rndne_f32_e32 v49, v49
	v_rndne_f32_e32 v50, v50
	v_cvt_i32_f32_e32 v47, v47
	v_cvt_i32_f32_sdwa v49, v49 dst_sel:WORD_1 dst_unused:UNUSED_PAD src0_sel:DWORD
	v_cvt_i32_f32_e32 v50, v50
	v_lshlrev_b32_e32 v48, 8, v48
	v_and_b32_e32 v48, 0xff00, v48
	v_and_b32_e32 v49, 0xff0000, v49
	v_perm_b32 v47, v50, v47, s65
	v_or3_b32 v47, v47, v48, v49
	v_lshlrev_b32_e32 v48, 16, v40
	v_and_b32_e32 v40, 0xffff0000, v40
	ds_write2st64_b32 v7, v57, v47 offset0:10 offset1:11
	v_lshlrev_b32_e32 v47, 16, v39
	v_lshlrev_b32_e32 v49, 16, v41
	v_lshlrev_b32_e32 v50, 16, v42
	v_and_b32_e32 v39, 0xffff0000, v39
	v_mul_f32_e32 v40, v2, v40
	v_and_b32_e32 v41, 0xffff0000, v41
	v_and_b32_e32 v42, 0xffff0000, v42
	v_mul_f32_e32 v39, v2, v39
	v_rndne_f32_e32 v40, v40
	v_mul_f32_e32 v41, v2, v41
	v_mul_f32_e32 v42, v2, v42
	v_rndne_f32_e32 v39, v39
	v_cvt_i32_f32_e32 v40, v40
	v_rndne_f32_e32 v41, v41
	v_rndne_f32_e32 v42, v42
	v_cvt_i32_f32_e32 v39, v39
	v_cvt_i32_f32_sdwa v41, v41 dst_sel:WORD_1 dst_unused:UNUSED_PAD src0_sel:DWORD
	v_cvt_i32_f32_e32 v42, v42
	v_lshlrev_b32_e32 v40, 8, v40
	v_and_b32_e32 v40, 0xff00, v40
	v_and_b32_e32 v41, 0xff0000, v41
	v_perm_b32 v39, v42, v39, s65
	v_or3_b32 v39, v39, v40, v41
	v_lshlrev_b32_e32 v40, 16, v44
	ds_write2st64_b32 v55, v51, v39 offset0:26 offset1:27
	v_lshlrev_b32_e32 v39, 16, v43
	v_mul_f32_e32 v40, v6, v40
	v_lshlrev_b32_e32 v41, 16, v45
	v_lshlrev_b32_e32 v42, 16, v46
	v_mul_f32_e32 v39, v6, v39
	v_rndne_f32_e32 v40, v40
	v_mul_f32_e32 v41, v6, v41
	v_mul_f32_e32 v42, v6, v42
	v_rndne_f32_e32 v39, v39
	v_cvt_i32_f32_e32 v40, v40
	v_rndne_f32_e32 v41, v41
	v_rndne_f32_e32 v42, v42
	v_cvt_i32_f32_e32 v39, v39
	v_cvt_i32_f32_sdwa v41, v41 dst_sel:WORD_1 dst_unused:UNUSED_PAD src0_sel:DWORD
	v_cvt_i32_f32_e32 v42, v42
	v_lshlrev_b32_e32 v40, 8, v40
	v_and_b32_e32 v40, 0xff00, v40
	v_and_b32_e32 v41, 0xff0000, v41
	v_perm_b32 v39, v42, v39, s65
	v_or3_b32 v39, v39, v40, v41
	v_and_b32_e32 v41, 0xffff0000, v44
	v_and_b32_e32 v40, 0xffff0000, v43
	v_mul_f32_e32 v41, v4, v41
	v_and_b32_e32 v42, 0xffff0000, v45
	v_and_b32_e32 v43, 0xffff0000, v46
	v_mul_f32_e32 v40, v4, v40
	v_rndne_f32_e32 v41, v41
	v_mul_f32_e32 v42, v4, v42
	v_mul_f32_e32 v43, v4, v43
	v_rndne_f32_e32 v40, v40
	v_cvt_i32_f32_e32 v41, v41
	v_rndne_f32_e32 v42, v42
	v_rndne_f32_e32 v43, v43
	v_cvt_i32_f32_e32 v40, v40
	v_cvt_i32_f32_sdwa v42, v42 dst_sel:WORD_1 dst_unused:UNUSED_PAD src0_sel:DWORD
	v_cvt_i32_f32_e32 v43, v43
	v_lshlrev_b32_e32 v41, 8, v41
	v_and_b32_e32 v41, 0xff00, v41
	v_and_b32_e32 v42, 0xff0000, v42
	v_perm_b32 v40, v43, v40, s65
	v_or3_b32 v40, v40, v41, v42
	v_lshlrev_b32_e32 v42, 16, v36
	v_and_b32_e32 v36, 0xffff0000, v36
	v_lshlrev_b32_e32 v41, 16, v35
	v_lshlrev_b32_e32 v43, 16, v37
	v_lshlrev_b32_e32 v44, 16, v38
	v_and_b32_e32 v35, 0xffff0000, v35
	v_mul_f32_e32 v36, v2, v36
	v_and_b32_e32 v37, 0xffff0000, v37
	v_and_b32_e32 v38, 0xffff0000, v38
	v_mul_f32_e32 v42, v3, v42
	v_mul_f32_e32 v35, v2, v35
	v_rndne_f32_e32 v36, v36
	v_mul_f32_e32 v37, v2, v37
	v_mul_f32_e32 v38, v2, v38
	v_mul_f32_e32 v41, v3, v41
	v_rndne_f32_e32 v42, v42
	v_mul_f32_e32 v43, v3, v43
	v_mul_f32_e32 v44, v3, v44
	v_rndne_f32_e32 v35, v35
	v_cvt_i32_f32_e32 v36, v36
	v_rndne_f32_e32 v37, v37
	v_rndne_f32_e32 v38, v38
	v_rndne_f32_e32 v41, v41
	v_cvt_i32_f32_e32 v42, v42
	v_rndne_f32_e32 v43, v43
	v_rndne_f32_e32 v44, v44
	v_cvt_i32_f32_e32 v35, v35
	v_cvt_i32_f32_sdwa v37, v37 dst_sel:WORD_1 dst_unused:UNUSED_PAD src0_sel:DWORD
	v_cvt_i32_f32_e32 v38, v38
	v_cvt_i32_f32_e32 v41, v41
	v_cvt_i32_f32_sdwa v43, v43 dst_sel:WORD_1 dst_unused:UNUSED_PAD src0_sel:DWORD
	v_cvt_i32_f32_e32 v44, v44
	v_lshlrev_b32_e32 v36, 8, v36
	v_lshlrev_b32_e32 v42, 8, v42
	v_and_b32_e32 v36, 0xff00, v36
	v_and_b32_e32 v37, 0xff0000, v37
	v_perm_b32 v35, v38, v35, s65
	v_and_b32_e32 v42, 0xff00, v42
	v_and_b32_e32 v43, 0xff0000, v43
	v_perm_b32 v41, v44, v41, s65
	v_or3_b32 v35, v35, v36, v37
	v_lshlrev_b32_e32 v37, 16, v32
	v_and_b32_e32 v32, 0xffff0000, v32
	v_or3_b32 v41, v41, v42, v43
	v_lshlrev_b32_e32 v36, 16, v31
	v_lshlrev_b32_e32 v38, 16, v33
	v_lshlrev_b32_e32 v42, 16, v34
	v_and_b32_e32 v31, 0xffff0000, v31
	v_mul_f32_e32 v32, v4, v32
	v_and_b32_e32 v33, 0xffff0000, v33
	v_and_b32_e32 v34, 0xffff0000, v34
	v_mul_f32_e32 v31, v4, v31
	v_rndne_f32_e32 v32, v32
	v_mul_f32_e32 v33, v4, v33
	v_mul_f32_e32 v34, v4, v34
	v_rndne_f32_e32 v31, v31
	v_cvt_i32_f32_e32 v32, v32
	v_rndne_f32_e32 v33, v33
	v_rndne_f32_e32 v34, v34
	v_cvt_i32_f32_e32 v31, v31
	v_cvt_i32_f32_sdwa v33, v33 dst_sel:WORD_1 dst_unused:UNUSED_PAD src0_sel:DWORD
	v_cvt_i32_f32_e32 v34, v34
	v_lshlrev_b32_e32 v32, 8, v32
	v_and_b32_e32 v32, 0xff00, v32
	v_and_b32_e32 v33, 0xff0000, v33
	v_perm_b32 v31, v34, v31, s65
	v_or3_b32 v31, v31, v32, v33
	v_lshlrev_b32_e32 v32, 16, v28
	v_and_b32_e32 v28, 0xffff0000, v28
	ds_write2st64_b32 v7, v40, v31 offset0:12 offset1:13
	v_lshlrev_b32_e32 v31, 16, v27
	v_lshlrev_b32_e32 v33, 16, v29
	v_lshlrev_b32_e32 v34, 16, v30
	v_and_b32_e32 v27, 0xffff0000, v27
	v_mul_f32_e32 v28, v2, v28
	v_and_b32_e32 v29, 0xffff0000, v29
	v_and_b32_e32 v30, 0xffff0000, v30
	v_mul_f32_e32 v27, v2, v27
	v_rndne_f32_e32 v28, v28
	v_mul_f32_e32 v29, v2, v29
	v_mul_f32_e32 v30, v2, v30
	v_rndne_f32_e32 v27, v27
	v_cvt_i32_f32_e32 v28, v28
	v_rndne_f32_e32 v29, v29
	v_rndne_f32_e32 v30, v30
	v_cvt_i32_f32_e32 v27, v27
	v_cvt_i32_f32_sdwa v29, v29 dst_sel:WORD_1 dst_unused:UNUSED_PAD src0_sel:DWORD
	v_cvt_i32_f32_e32 v30, v30
	v_lshlrev_b32_e32 v28, 8, v28
	v_and_b32_e32 v28, 0xff00, v28
	v_and_b32_e32 v29, 0xff0000, v29
	v_perm_b32 v27, v30, v27, s65
	v_or3_b32 v27, v27, v28, v29
	v_lshlrev_b32_e32 v28, 16, v24
	v_and_b32_e32 v24, 0xffff0000, v24
	ds_write2st64_b32 v55, v35, v27 offset0:28 offset1:29
	v_lshlrev_b32_e32 v27, 16, v23
	v_lshlrev_b32_e32 v29, 16, v25
	v_lshlrev_b32_e32 v30, 16, v26
	v_and_b32_e32 v23, 0xffff0000, v23
	v_mul_f32_e32 v24, v4, v24
	v_and_b32_e32 v25, 0xffff0000, v25
	v_and_b32_e32 v26, 0xffff0000, v26
	v_mul_f32_e32 v28, v6, v28
	v_mul_f32_e32 v23, v4, v23
	v_rndne_f32_e32 v24, v24
	v_mul_f32_e32 v25, v4, v25
	v_mul_f32_e32 v26, v4, v26
	v_mul_f32_e32 v27, v6, v27
	v_rndne_f32_e32 v28, v28
	v_mul_f32_e32 v29, v6, v29
	v_mul_f32_e32 v30, v6, v30
	v_rndne_f32_e32 v23, v23
	v_cvt_i32_f32_e32 v24, v24
	v_rndne_f32_e32 v25, v25
	v_rndne_f32_e32 v26, v26
	v_rndne_f32_e32 v27, v27
	v_cvt_i32_f32_e32 v28, v28
	v_rndne_f32_e32 v29, v29
	v_rndne_f32_e32 v30, v30
	v_cvt_i32_f32_e32 v23, v23
	v_cvt_i32_f32_sdwa v25, v25 dst_sel:WORD_1 dst_unused:UNUSED_PAD src0_sel:DWORD
	v_cvt_i32_f32_e32 v26, v26
	v_cvt_i32_f32_e32 v27, v27
	v_cvt_i32_f32_sdwa v29, v29 dst_sel:WORD_1 dst_unused:UNUSED_PAD src0_sel:DWORD
	v_cvt_i32_f32_e32 v30, v30
	v_lshlrev_b32_e32 v24, 8, v24
	v_lshlrev_b32_e32 v28, 8, v28
	v_and_b32_e32 v24, 0xff00, v24
	v_and_b32_e32 v25, 0xff0000, v25
	v_perm_b32 v23, v26, v23, s65
	v_and_b32_e32 v28, 0xff00, v28
	v_and_b32_e32 v29, 0xff0000, v29
	v_perm_b32 v27, v30, v27, s65
	v_or3_b32 v23, v23, v24, v25
	v_lshlrev_b32_e32 v25, 16, v19
	v_and_b32_e32 v19, 0xffff0000, v19
	v_or3_b32 v27, v27, v28, v29
	v_lshlrev_b32_e32 v24, 16, v18
	v_lshlrev_b32_e32 v26, 16, v20
	v_lshlrev_b32_e32 v28, 16, v21
	v_and_b32_e32 v18, 0xffff0000, v18
	v_mul_f32_e32 v19, v2, v19
	v_and_b32_e32 v20, 0xffff0000, v20
	v_and_b32_e32 v21, 0xffff0000, v21
	v_mul_f32_e32 v25, v3, v25
	v_mul_f32_e32 v18, v2, v18
	v_rndne_f32_e32 v19, v19
	v_mul_f32_e32 v20, v2, v20
	v_mul_f32_e32 v21, v2, v21
	v_mul_f32_e32 v24, v3, v24
	v_rndne_f32_e32 v25, v25
	v_mul_f32_e32 v26, v3, v26
	v_mul_f32_e32 v28, v3, v28
	v_rndne_f32_e32 v18, v18
	v_cvt_i32_f32_e32 v19, v19
	v_rndne_f32_e32 v20, v20
	v_rndne_f32_e32 v21, v21
	v_rndne_f32_e32 v24, v24
	v_cvt_i32_f32_e32 v25, v25
	v_rndne_f32_e32 v26, v26
	v_rndne_f32_e32 v28, v28
	v_cvt_i32_f32_e32 v18, v18
	v_cvt_i32_f32_sdwa v20, v20 dst_sel:WORD_1 dst_unused:UNUSED_PAD src0_sel:DWORD
	v_cvt_i32_f32_e32 v21, v21
	v_cvt_i32_f32_e32 v24, v24
	v_cvt_i32_f32_sdwa v26, v26 dst_sel:WORD_1 dst_unused:UNUSED_PAD src0_sel:DWORD
	v_cvt_i32_f32_e32 v28, v28
	v_lshlrev_b32_e32 v19, 8, v19
	v_lshlrev_b32_e32 v25, 8, v25
	v_and_b32_e32 v19, 0xff00, v19
	v_and_b32_e32 v20, 0xff0000, v20
	v_perm_b32 v18, v21, v18, s65
	v_and_b32_e32 v25, 0xff00, v25
	v_and_b32_e32 v26, 0xff0000, v26
	v_perm_b32 v24, v28, v24, s65
	v_or3_b32 v18, v18, v19, v20
	v_lshlrev_b32_e32 v20, 16, v15
	v_or3_b32 v24, v24, v25, v26
	v_lshlrev_b32_e32 v19, 16, v14
	v_mul_f32_e32 v20, v6, v20
	v_lshlrev_b32_e32 v21, 16, v16
	v_lshlrev_b32_e32 v25, 16, v17
	v_mul_f32_e32 v52, v6, v52
	v_mul_f32_e32 v53, v6, v53
	v_mul_f32_e32 v54, v6, v54
	v_mul_f32_e32 v59, v6, v59
	v_mul_f32_e32 v36, v6, v36
	v_mul_f32_e32 v37, v6, v37
	v_mul_f32_e32 v38, v6, v38
	v_mul_f32_e32 v42, v6, v42
	v_mul_f32_e32 v19, v6, v19
	v_rndne_f32_e32 v20, v20
	v_mul_f32_e32 v21, v6, v21
	v_mul_f32_e32 v6, v6, v25
	v_rndne_f32_e32 v53, v53
	v_rndne_f32_e32 v37, v37
	v_rndne_f32_e32 v19, v19
	v_cvt_i32_f32_e32 v20, v20
	v_rndne_f32_e32 v21, v21
	v_rndne_f32_e32 v6, v6
	v_rndne_f32_e32 v52, v52
	v_cvt_i32_f32_e32 v53, v53
	v_rndne_f32_e32 v54, v54
	v_rndne_f32_e32 v59, v59
	v_rndne_f32_e32 v36, v36
	v_cvt_i32_f32_e32 v37, v37
	v_rndne_f32_e32 v38, v38
	v_rndne_f32_e32 v42, v42
	v_cvt_i32_f32_e32 v19, v19
	v_cvt_i32_f32_sdwa v21, v21 dst_sel:WORD_1 dst_unused:UNUSED_PAD src0_sel:DWORD
	v_cvt_i32_f32_e32 v6, v6
	v_cvt_i32_f32_e32 v52, v52
	v_cvt_i32_f32_sdwa v54, v54 dst_sel:WORD_1 dst_unused:UNUSED_PAD src0_sel:DWORD
	v_cvt_i32_f32_e32 v59, v59
	v_cvt_i32_f32_e32 v36, v36
	v_cvt_i32_f32_sdwa v38, v38 dst_sel:WORD_1 dst_unused:UNUSED_PAD src0_sel:DWORD
	v_cvt_i32_f32_e32 v42, v42
	v_lshlrev_b32_e32 v20, 8, v20
	v_lshlrev_b32_e32 v53, 8, v53
	v_lshlrev_b32_e32 v37, 8, v37
	v_and_b32_e32 v20, 0xff00, v20
	v_and_b32_e32 v21, 0xff0000, v21
	v_perm_b32 v6, v6, v19, s65
	v_and_b32_e32 v53, 0xff00, v53
	v_and_b32_e32 v54, 0xff0000, v54
	v_perm_b32 v52, v59, v52, s65
	v_and_b32_e32 v37, 0xff00, v37
	v_and_b32_e32 v38, 0xff0000, v38
	v_perm_b32 v36, v42, v36, s65
	v_or3_b32 v6, v6, v20, v21
	v_or3_b32 v52, v52, v53, v54
	v_or3_b32 v36, v36, v37, v38
	ds_write2st64_b32 v5, v27, v6 offset0:6 offset1:7
	v_and_b32_e32 v6, 0xffff0000, v15
	ds_write2st64_b32 v5, v56, v52 offset0:2 offset1:3
	ds_write2st64_b32 v5, v39, v36 offset0:4 offset1:5
	v_and_b32_e32 v5, 0xffff0000, v14
	v_mul_f32_e32 v6, v4, v6
	v_and_b32_e32 v14, 0xffff0000, v16
	v_and_b32_e32 v15, 0xffff0000, v17
	v_mul_f32_e32 v5, v4, v5
	v_rndne_f32_e32 v6, v6
	v_mul_f32_e32 v14, v4, v14
	v_mul_f32_e32 v4, v4, v15
	v_rndne_f32_e32 v5, v5
	v_cvt_i32_f32_e32 v6, v6
	v_rndne_f32_e32 v14, v14
	v_rndne_f32_e32 v4, v4
	v_cvt_i32_f32_e32 v5, v5
	v_cvt_i32_f32_sdwa v14, v14 dst_sel:WORD_1 dst_unused:UNUSED_PAD src0_sel:DWORD
	v_cvt_i32_f32_e32 v4, v4
	v_lshlrev_b32_e32 v6, 8, v6
	v_and_b32_e32 v6, 0xff00, v6
	v_and_b32_e32 v14, 0xff0000, v14
	v_perm_b32 v4, v4, v5, s65
	v_or3_b32 v4, v4, v6, v14
	v_lshlrev_b32_e32 v5, 16, v10
	ds_write2st64_b32 v7, v23, v4 offset0:14 offset1:15
	v_lshlrev_b32_e32 v4, 16, v9
	v_mul_f32_e32 v5, v3, v5
	v_lshlrev_b32_e32 v6, 16, v12
	v_lshlrev_b32_e32 v7, 16, v13
	v_mul_f32_e32 v47, v3, v47
	v_mul_f32_e32 v48, v3, v48
	v_mul_f32_e32 v49, v3, v49
	v_mul_f32_e32 v50, v3, v50
	v_mul_f32_e32 v31, v3, v31
	v_mul_f32_e32 v32, v3, v32
	v_mul_f32_e32 v33, v3, v33
	v_mul_f32_e32 v34, v3, v34
	v_mul_f32_e32 v4, v3, v4
	v_rndne_f32_e32 v5, v5
	v_mul_f32_e32 v6, v3, v6
	v_mul_f32_e32 v3, v3, v7
	v_rndne_f32_e32 v4, v4
	v_cvt_i32_f32_e32 v5, v5
	v_rndne_f32_e32 v6, v6
	v_rndne_f32_e32 v3, v3
	v_cvt_i32_f32_e32 v4, v4
	v_cvt_i32_f32_sdwa v6, v6 dst_sel:WORD_1 dst_unused:UNUSED_PAD src0_sel:DWORD
	v_cvt_i32_f32_e32 v3, v3
	v_lshlrev_b32_e32 v5, 8, v5
	v_and_b32_e32 v5, 0xff00, v5
	v_and_b32_e32 v6, 0xff0000, v6
	v_perm_b32 v3, v3, v4, s65
	v_or3_b32 v3, v3, v5, v6
	v_and_b32_e32 v4, 0xffff0000, v10
	ds_write2st64_b32 v22, v24, v3 offset0:22 offset1:23
	v_and_b32_e32 v3, 0xffff0000, v9
	v_mul_f32_e32 v4, v2, v4
	v_and_b32_e32 v5, 0xffff0000, v12
	v_and_b32_e32 v6, 0xffff0000, v13
	v_rndne_f32_e32 v48, v48
	v_rndne_f32_e32 v32, v32
	v_mul_f32_e32 v3, v2, v3
	v_rndne_f32_e32 v4, v4
	v_mul_f32_e32 v5, v2, v5
	v_mul_f32_e32 v2, v2, v6
	v_rndne_f32_e32 v47, v47
	v_cvt_i32_f32_e32 v48, v48
	v_rndne_f32_e32 v49, v49
	v_rndne_f32_e32 v50, v50
	v_rndne_f32_e32 v31, v31
	v_cvt_i32_f32_e32 v32, v32
	v_rndne_f32_e32 v33, v33
	v_rndne_f32_e32 v34, v34
	v_rndne_f32_e32 v3, v3
	v_cvt_i32_f32_e32 v4, v4
	v_rndne_f32_e32 v5, v5
	v_rndne_f32_e32 v2, v2
	v_cvt_i32_f32_e32 v47, v47
	v_cvt_i32_f32_sdwa v49, v49 dst_sel:WORD_1 dst_unused:UNUSED_PAD src0_sel:DWORD
	v_cvt_i32_f32_e32 v50, v50
	v_cvt_i32_f32_e32 v31, v31
	v_cvt_i32_f32_sdwa v33, v33 dst_sel:WORD_1 dst_unused:UNUSED_PAD src0_sel:DWORD
	v_cvt_i32_f32_e32 v34, v34
	v_cvt_i32_f32_e32 v3, v3
	v_cvt_i32_f32_sdwa v5, v5 dst_sel:WORD_1 dst_unused:UNUSED_PAD src0_sel:DWORD
	v_cvt_i32_f32_e32 v2, v2
	v_lshlrev_b32_e32 v48, 8, v48
	v_lshlrev_b32_e32 v32, 8, v32
	v_lshlrev_b32_e32 v4, 8, v4
	v_and_b32_e32 v48, 0xff00, v48
	v_and_b32_e32 v49, 0xff0000, v49
	v_perm_b32 v47, v50, v47, s65
	v_and_b32_e32 v32, 0xff00, v32
	v_and_b32_e32 v33, 0xff0000, v33
	v_perm_b32 v31, v34, v31, s65
	v_and_b32_e32 v4, 0xff00, v4
	v_and_b32_e32 v5, 0xff0000, v5
	v_perm_b32 v2, v2, v3, s65
	v_or3_b32 v47, v47, v48, v49
	v_or3_b32 v31, v31, v32, v33
	v_or3_b32 v2, v2, v4, v5
	ds_write2st64_b32 v22, v58, v47 offset0:18 offset1:19
	ds_write2st64_b32 v22, v41, v31 offset0:20 offset1:21
	ds_write2st64_b32 v55, v18, v2 offset0:30 offset1:31
	s_waitcnt lgkmcnt(0)
	s_barrier
	v_cmp_eq_u32_e32 vcc, 0, v0
	s_and_saveexec_b64 s[98:99], vcc
	v_mov_b32_e32 v200, 1
	s_nop 0
	global_atomic_add v200, v11, v200, s[16:17] sc0
	s_mov_b64 exec, s[98:99]
	v_cmp_gt_i32_e32 vcc, s66, v8
	s_and_saveexec_b64 s[4:5], vcc
	s_cbranch_execz .LBB0_223
	s_and_b64 s[6:7], s[6:7], exec
	s_cselect_b32 s6, 0xc80000, 0
	v_readlane_b32 s8, v252, 15
	v_readlane_b32 s9, v252, 16
	s_add_u32 s6, s8, s6
	s_addc_u32 s7, s9, 0
	v_lshlrev_b32_e32 v2, 4, v8
	s_mov_b64 s[8:9], 0

.LBB0_235:
	s_or_b64 exec, exec, s[10:11]
	s_nop 0
	v_max_f32_e32 v2, v2, v2
	v_max_f32_e32 v2, 0xda24260, v2
	v_div_scale_f32 v50, s[8:9], v2, v2, s63
	v_rcp_f32_e32 v75, v50
	v_div_scale_f32 v76, vcc, s63, v2, s63
	v_max_f32_e32 v3, v3, v3
	v_fma_f32 v77, -v50, v75, 1.0
	v_fmac_f32_e32 v75, v77, v75
	v_mul_f32_e32 v77, v76, v75
	v_fma_f32 v94, -v50, v77, v76
	v_fmac_f32_e32 v77, v94, v75
	v_max_f32_e32 v3, 0xda24260, v3
	v_fma_f32 v50, -v50, v77, v76
	v_div_scale_f32 v76, s[8:9], v3, v3, s63
	v_rcp_f32_e32 v94, v76
	v_div_fmas_f32 v50, v50, v75, v77
	v_div_fixup_f32 v50, v50, v2, s63
	v_max_f32_e32 v4, v4, v4
	v_fma_f32 v2, -v76, v94, 1.0
	v_fmac_f32_e32 v94, v2, v94
	v_div_scale_f32 v2, vcc, s63, v3, s63
	v_mul_f32_e32 v75, v2, v94
	v_fma_f32 v77, -v76, v75, v2
	v_fmac_f32_e32 v75, v77, v94
	v_fma_f32 v2, -v76, v75, v2
	v_max_f32_e32 v76, 0xda24260, v4
	v_div_scale_f32 v77, s[8:9], v76, v76, s63
	v_rcp_f32_e32 v95, v77
	v_div_fmas_f32 v2, v2, v94, v75
	v_div_fixup_f32 v4, v2, v3, s63
	v_max_f32_e32 v5, v5, v5
	v_fma_f32 v2, -v77, v95, 1.0
	v_fmac_f32_e32 v95, v2, v95
	v_div_scale_f32 v2, vcc, s63, v76, s63
	v_mul_f32_e32 v3, v2, v95
	v_fma_f32 v75, -v77, v3, v2
	v_max_f32_e32 v5, 0xda24260, v5
	v_fmac_f32_e32 v3, v75, v95
	v_div_scale_f32 v75, s[8:9], v5, v5, s63
	v_fma_f32 v2, -v77, v3, v2
	v_rcp_f32_e32 v77, v75
	v_div_fmas_f32 v2, v2, v95, v3
	v_div_fixup_f32 v3, v2, v76, s63
	v_fma_f32 v2, -v75, v77, 1.0
	v_fmac_f32_e32 v77, v2, v77
	v_div_scale_f32 v2, vcc, s63, v5, s63
	v_mul_f32_e32 v76, v2, v77
	v_fma_f32 v94, -v75, v76, v2
	v_fmac_f32_e32 v76, v94, v77
	v_fma_f32 v2, -v75, v76, v2
	v_div_fmas_f32 v2, v2, v77, v76
	v_div_fixup_f32 v2, v2, v5, s63
	v_mul_lo_u32 v5, v57, s64
	v_add3_u32 v5, 0, v5, v58
	v_lshlrev_b32_e32 v58, 16, v72
	v_lshlrev_b32_e32 v57, 16, v71
	v_mul_f32_e32 v58, v50, v58
	v_lshlrev_b32_e32 v75, 16, v73
	v_lshlrev_b32_e32 v76, 16, v74
	v_mul_f32_e32 v57, v50, v57
	v_rndne_f32_e32 v58, v58
	v_mul_f32_e32 v75, v50, v75
	v_mul_f32_e32 v76, v50, v76
	v_rndne_f32_e32 v57, v57
	v_cvt_i32_f32_e32 v58, v58
	v_rndne_f32_e32 v75, v75
	v_rndne_f32_e32 v76, v76
	v_cvt_i32_f32_e32 v57, v57
	v_cvt_i32_f32_sdwa v75, v75 dst_sel:WORD_1 dst_unused:UNUSED_PAD src0_sel:DWORD
	v_cvt_i32_f32_e32 v76, v76
	v_lshlrev_b32_e32 v58, 8, v58
	v_and_b32_e32 v58, 0xff00, v58
	v_and_b32_e32 v75, 0xff0000, v75
	v_perm_b32 v57, v76, v57, s65
	v_or3_b32 v57, v57, v58, v75
	v_and_b32_e32 v58, 0xffff0000, v71
	v_and_b32_e32 v71, 0xffff0000, v72
	v_mul_f32_e32 v71, v4, v71
	v_and_b32_e32 v72, 0xffff0000, v73
	v_and_b32_e32 v73, 0xffff0000, v74
	v_mul_f32_e32 v58, v4, v58
	v_rndne_f32_e32 v71, v71
	v_mul_f32_e32 v72, v4, v72
	v_mul_f32_e32 v73, v4, v73
	v_rndne_f32_e32 v58, v58
	v_cvt_i32_f32_e32 v71, v71
	v_rndne_f32_e32 v72, v72
	v_rndne_f32_e32 v73, v73
	v_cvt_i32_f32_e32 v58, v58
	v_cvt_i32_f32_sdwa v72, v72 dst_sel:WORD_1 dst_unused:UNUSED_PAD src0_sel:DWORD
	v_cvt_i32_f32_e32 v73, v73
	v_lshlrev_b32_e32 v71, 8, v71
	v_and_b32_e32 v71, 0xff00, v71
	v_and_b32_e32 v72, 0xff0000, v72
	v_perm_b32 v58, v73, v58, s65
	v_or3_b32 v58, v58, v71, v72
	v_lshlrev_b32_e32 v72, 16, v68
	v_and_b32_e32 v68, 0xffff0000, v68
	v_lshlrev_b32_e32 v71, 16, v67
	v_lshlrev_b32_e32 v73, 16, v69
	v_lshlrev_b32_e32 v74, 16, v70
	v_and_b32_e32 v67, 0xffff0000, v67
	v_mul_f32_e32 v68, v2, v68
	v_and_b32_e32 v69, 0xffff0000, v69
	v_and_b32_e32 v70, 0xffff0000, v70
	v_mul_f32_e32 v72, v3, v72
	v_mul_f32_e32 v67, v2, v67
	v_rndne_f32_e32 v68, v68
	v_mul_f32_e32 v69, v2, v69
	v_mul_f32_e32 v70, v2, v70
	v_mul_f32_e32 v71, v3, v71
	v_rndne_f32_e32 v72, v72
	v_mul_f32_e32 v73, v3, v73
	v_mul_f32_e32 v74, v3, v74
	v_rndne_f32_e32 v67, v67
	v_cvt_i32_f32_e32 v68, v68
	v_rndne_f32_e32 v69, v69
	v_rndne_f32_e32 v70, v70
	v_rndne_f32_e32 v71, v71
	v_cvt_i32_f32_e32 v72, v72
	v_rndne_f32_e32 v73, v73
	v_rndne_f32_e32 v74, v74
	v_cvt_i32_f32_e32 v67, v67
	v_cvt_i32_f32_sdwa v69, v69 dst_sel:WORD_1 dst_unused:UNUSED_PAD src0_sel:DWORD
	v_cvt_i32_f32_e32 v70, v70
	v_cvt_i32_f32_e32 v71, v71
	v_cvt_i32_f32_sdwa v73, v73 dst_sel:WORD_1 dst_unused:UNUSED_PAD src0_sel:DWORD
	v_cvt_i32_f32_e32 v74, v74
	v_lshlrev_b32_e32 v68, 8, v68
	v_lshlrev_b32_e32 v72, 8, v72
	v_and_b32_e32 v68, 0xff00, v68
	v_and_b32_e32 v69, 0xff0000, v69
	v_perm_b32 v67, v70, v67, s65
	v_and_b32_e32 v72, 0xff00, v72
	v_and_b32_e32 v73, 0xff0000, v73
	v_perm_b32 v71, v74, v71, s65
	v_or3_b32 v67, v67, v68, v69
	v_lshlrev_b32_e32 v69, 16, v64
	v_or3_b32 v71, v71, v72, v73
	v_lshlrev_b32_e32 v68, 16, v63
	v_mul_f32_e32 v69, v50, v69
	v_lshlrev_b32_e32 v70, 16, v65
	v_lshlrev_b32_e32 v72, 16, v66
	v_mul_f32_e32 v68, v50, v68
	v_rndne_f32_e32 v69, v69
	v_mul_f32_e32 v70, v50, v70
	v_mul_f32_e32 v72, v50, v72
	v_rndne_f32_e32 v68, v68
	v_cvt_i32_f32_e32 v69, v69
	v_rndne_f32_e32 v70, v70
	v_rndne_f32_e32 v72, v72
	v_cvt_i32_f32_e32 v68, v68
	v_cvt_i32_f32_sdwa v70, v70 dst_sel:WORD_1 dst_unused:UNUSED_PAD src0_sel:DWORD
	v_cvt_i32_f32_e32 v72, v72
	v_lshlrev_b32_e32 v69, 8, v69
	v_and_b32_e32 v69, 0xff00, v69
	v_and_b32_e32 v70, 0xff0000, v70
	v_perm_b32 v68, v72, v68, s65
	v_or3_b32 v68, v68, v69, v70
	ds_write2st64_b32 v5, v57, v68 offset1:1
	v_and_b32_e32 v57, 0xffff0000, v63
	v_and_b32_e32 v63, 0xffff0000, v64
	v_mul_f32_e32 v63, v4, v63
	v_and_b32_e32 v64, 0xffff0000, v65
	v_and_b32_e32 v65, 0xffff0000, v66
	v_mul_f32_e32 v57, v4, v57
	v_rndne_f32_e32 v63, v63
	v_mul_f32_e32 v64, v4, v64
	v_mul_f32_e32 v65, v4, v65
	v_rndne_f32_e32 v57, v57
	v_cvt_i32_f32_e32 v63, v63
	v_rndne_f32_e32 v64, v64
	v_rndne_f32_e32 v65, v65
	v_cvt_i32_f32_e32 v57, v57
	v_cvt_i32_f32_sdwa v64, v64 dst_sel:WORD_1 dst_unused:UNUSED_PAD src0_sel:DWORD
	v_cvt_i32_f32_e32 v65, v65
	v_lshlrev_b32_e32 v63, 8, v63
	v_and_b32_e32 v63, 0xff00, v63
	v_and_b32_e32 v64, 0xff0000, v64
	v_perm_b32 v57, v65, v57, s65
	v_or3_b32 v63, v57, v63, v64
	v_add_u32_e32 v57, 16, v5
	ds_write2st64_b32 v57, v58, v63 offset0:8 offset1:9
	v_lshlrev_b32_e32 v63, 16, v54
	v_and_b32_e32 v54, 0xffff0000, v54
	v_lshlrev_b32_e32 v58, 16, v53
	v_mul_f32_e32 v63, v3, v63
	v_lshlrev_b32_e32 v64, 16, v55
	v_lshlrev_b32_e32 v65, 16, v56
	v_and_b32_e32 v53, 0xffff0000, v53
	v_mul_f32_e32 v54, v2, v54
	v_and_b32_e32 v55, 0xffff0000, v55
	v_and_b32_e32 v56, 0xffff0000, v56
	v_mul_f32_e32 v58, v3, v58
	v_rndne_f32_e32 v63, v63
	v_mul_f32_e32 v64, v3, v64
	v_mul_f32_e32 v65, v3, v65
	v_mul_f32_e32 v53, v2, v53
	v_rndne_f32_e32 v54, v54
	v_mul_f32_e32 v55, v2, v55
	v_mul_f32_e32 v56, v2, v56
	v_rndne_f32_e32 v58, v58
	v_cvt_i32_f32_e32 v63, v63
	v_rndne_f32_e32 v64, v64
	v_rndne_f32_e32 v65, v65
	v_rndne_f32_e32 v53, v53
	v_cvt_i32_f32_e32 v54, v54
	v_rndne_f32_e32 v55, v55
	v_rndne_f32_e32 v56, v56
	v_cvt_i32_f32_e32 v58, v58
	v_cvt_i32_f32_sdwa v64, v64 dst_sel:WORD_1 dst_unused:UNUSED_PAD src0_sel:DWORD
	v_cvt_i32_f32_e32 v65, v65
	v_cvt_i32_f32_e32 v53, v53
	v_cvt_i32_f32_sdwa v55, v55 dst_sel:WORD_1 dst_unused:UNUSED_PAD src0_sel:DWORD
	v_cvt_i32_f32_e32 v56, v56
	v_lshlrev_b32_e32 v63, 8, v63
	v_lshlrev_b32_e32 v54, 8, v54
	v_and_b32_e32 v63, 0xff00, v63
	v_and_b32_e32 v64, 0xff0000, v64
	v_perm_b32 v58, v65, v58, s65
	v_and_b32_e32 v54, 0xff00, v54
	v_and_b32_e32 v55, 0xff0000, v55
	v_perm_b32 v53, v56, v53, s65
	v_or3_b32 v63, v58, v63, v64
	v_add_u32_e32 v58, 32, v5
	v_or3_b32 v54, v53, v54, v55
	v_add_u32_e32 v53, 48, v5
	v_lshlrev_b32_e32 v55, 16, v60
	ds_write2st64_b32 v58, v71, v63 offset0:16 offset1:17
	ds_write2st64_b32 v53, v67, v54 offset0:24 offset1:25
	v_lshlrev_b32_e32 v54, 16, v59
	v_mul_f32_e32 v55, v50, v55
	v_lshlrev_b32_e32 v56, 16, v61
	v_lshlrev_b32_e32 v63, 16, v62
	v_mul_f32_e32 v54, v50, v54
	v_rndne_f32_e32 v55, v55
	v_mul_f32_e32 v56, v50, v56
	v_mul_f32_e32 v63, v50, v63
	v_rndne_f32_e32 v54, v54
	v_cvt_i32_f32_e32 v55, v55
	v_rndne_f32_e32 v56, v56
	v_rndne_f32_e32 v63, v63
	v_cvt_i32_f32_e32 v54, v54
	v_cvt_i32_f32_sdwa v56, v56 dst_sel:WORD_1 dst_unused:UNUSED_PAD src0_sel:DWORD
	v_cvt_i32_f32_e32 v63, v63
	v_lshlrev_b32_e32 v55, 8, v55
	v_and_b32_e32 v55, 0xff00, v55
	v_and_b32_e32 v56, 0xff0000, v56
	v_perm_b32 v54, v63, v54, s65
	v_or3_b32 v54, v54, v55, v56
	v_and_b32_e32 v56, 0xffff0000, v60
	v_and_b32_e32 v55, 0xffff0000, v59
	v_mul_f32_e32 v56, v4, v56
	v_and_b32_e32 v59, 0xffff0000, v61
	v_and_b32_e32 v60, 0xffff0000, v62
	v_mul_f32_e32 v55, v4, v55
	v_rndne_f32_e32 v56, v56
	v_mul_f32_e32 v59, v4, v59
	v_mul_f32_e32 v60, v4, v60
	v_rndne_f32_e32 v55, v55
	v_cvt_i32_f32_e32 v56, v56
	v_rndne_f32_e32 v59, v59
	v_rndne_f32_e32 v60, v60
	v_cvt_i32_f32_e32 v55, v55
	v_cvt_i32_f32_sdwa v59, v59 dst_sel:WORD_1 dst_unused:UNUSED_PAD src0_sel:DWORD
	v_cvt_i32_f32_e32 v60, v60
	v_lshlrev_b32_e32 v56, 8, v56
	v_and_b32_e32 v56, 0xff00, v56
	v_and_b32_e32 v59, 0xff0000, v59
	v_perm_b32 v55, v60, v55, s65
	v_or3_b32 v55, v55, v56, v59
	v_lshlrev_b32_e32 v59, 16, v49
	v_and_b32_e32 v49, 0xffff0000, v49
	v_lshlrev_b32_e32 v56, 16, v48
	v_lshlrev_b32_e32 v60, 16, v51
	v_lshlrev_b32_e32 v61, 16, v52
	v_and_b32_e32 v48, 0xffff0000, v48
	v_mul_f32_e32 v49, v2, v49
	v_and_b32_e32 v51, 0xffff0000, v51
	v_and_b32_e32 v52, 0xffff0000, v52
	v_mul_f32_e32 v59, v3, v59
	v_mul_f32_e32 v48, v2, v48
	v_rndne_f32_e32 v49, v49
	v_mul_f32_e32 v51, v2, v51
	v_mul_f32_e32 v52, v2, v52
	v_mul_f32_e32 v56, v3, v56
	v_rndne_f32_e32 v59, v59
	v_mul_f32_e32 v60, v3, v60
	v_mul_f32_e32 v61, v3, v61
	v_rndne_f32_e32 v48, v48
	v_cvt_i32_f32_e32 v49, v49
	v_rndne_f32_e32 v51, v51
	v_rndne_f32_e32 v52, v52
	v_rndne_f32_e32 v56, v56
	v_cvt_i32_f32_e32 v59, v59
	v_rndne_f32_e32 v60, v60
	v_rndne_f32_e32 v61, v61
	v_cvt_i32_f32_e32 v48, v48
	v_cvt_i32_f32_sdwa v51, v51 dst_sel:WORD_1 dst_unused:UNUSED_PAD src0_sel:DWORD
	v_cvt_i32_f32_e32 v52, v52
	v_cvt_i32_f32_e32 v56, v56
	v_cvt_i32_f32_sdwa v60, v60 dst_sel:WORD_1 dst_unused:UNUSED_PAD src0_sel:DWORD
	v_cvt_i32_f32_e32 v61, v61
	v_lshlrev_b32_e32 v49, 8, v49
	v_lshlrev_b32_e32 v59, 8, v59
	v_and_b32_e32 v49, 0xff00, v49
	v_and_b32_e32 v51, 0xff0000, v51
	v_perm_b32 v48, v52, v48, s65
	v_and_b32_e32 v59, 0xff00, v59
	v_and_b32_e32 v60, 0xff0000, v60
	v_perm_b32 v56, v61, v56, s65
	v_or3_b32 v48, v48, v49, v51
	v_lshlrev_b32_e32 v51, 16, v45
	v_and_b32_e32 v45, 0xffff0000, v45
	v_or3_b32 v56, v56, v59, v60
	v_lshlrev_b32_e32 v49, 16, v44
	v_lshlrev_b32_e32 v52, 16, v46
	v_lshlrev_b32_e32 v59, 16, v47
	v_and_b32_e32 v44, 0xffff0000, v44
	v_mul_f32_e32 v45, v4, v45
	v_and_b32_e32 v46, 0xffff0000, v46
	v_and_b32_e32 v47, 0xffff0000, v47
	v_mul_f32_e32 v44, v4, v44
	v_rndne_f32_e32 v45, v45
	v_mul_f32_e32 v46, v4, v46
	v_mul_f32_e32 v47, v4, v47
	v_rndne_f32_e32 v44, v44
	v_cvt_i32_f32_e32 v45, v45
	v_rndne_f32_e32 v46, v46
	v_rndne_f32_e32 v47, v47
	v_cvt_i32_f32_e32 v44, v44
	v_cvt_i32_f32_sdwa v46, v46 dst_sel:WORD_1 dst_unused:UNUSED_PAD src0_sel:DWORD
	v_cvt_i32_f32_e32 v47, v47
	v_lshlrev_b32_e32 v45, 8, v45
	v_and_b32_e32 v45, 0xff00, v45
	v_and_b32_e32 v46, 0xff0000, v46
	v_perm_b32 v44, v47, v44, s65
	v_or3_b32 v44, v44, v45, v46
	v_lshlrev_b32_e32 v45, 16, v37
	v_and_b32_e32 v37, 0xffff0000, v37
	ds_write2st64_b32 v57, v55, v44 offset0:10 offset1:11
	v_lshlrev_b32_e32 v44, 16, v36
	v_lshlrev_b32_e32 v46, 16, v38
	v_lshlrev_b32_e32 v47, 16, v39
	v_and_b32_e32 v36, 0xffff0000, v36
	v_mul_f32_e32 v37, v2, v37
	v_and_b32_e32 v38, 0xffff0000, v38
	v_and_b32_e32 v39, 0xffff0000, v39
	v_mul_f32_e32 v36, v2, v36
	v_rndne_f32_e32 v37, v37
	v_mul_f32_e32 v38, v2, v38
	v_mul_f32_e32 v39, v2, v39
	v_rndne_f32_e32 v36, v36
	v_cvt_i32_f32_e32 v37, v37
	v_rndne_f32_e32 v38, v38
	v_rndne_f32_e32 v39, v39
	v_cvt_i32_f32_e32 v36, v36
	v_cvt_i32_f32_sdwa v38, v38 dst_sel:WORD_1 dst_unused:UNUSED_PAD src0_sel:DWORD
	v_cvt_i32_f32_e32 v39, v39
	v_lshlrev_b32_e32 v37, 8, v37
	v_and_b32_e32 v37, 0xff00, v37
	v_and_b32_e32 v38, 0xff0000, v38
	v_perm_b32 v36, v39, v36, s65
	v_or3_b32 v36, v36, v37, v38
	v_lshlrev_b32_e32 v37, 16, v41
	ds_write2st64_b32 v53, v48, v36 offset0:26 offset1:27
	v_lshlrev_b32_e32 v36, 16, v40
	v_mul_f32_e32 v37, v50, v37
	v_lshlrev_b32_e32 v38, 16, v42
	v_lshlrev_b32_e32 v39, 16, v43
	v_mul_f32_e32 v36, v50, v36
	v_rndne_f32_e32 v37, v37
	v_mul_f32_e32 v38, v50, v38
	v_mul_f32_e32 v39, v50, v39
	v_rndne_f32_e32 v36, v36
	v_cvt_i32_f32_e32 v37, v37
	v_rndne_f32_e32 v38, v38
	v_rndne_f32_e32 v39, v39
	v_cvt_i32_f32_e32 v36, v36
	v_cvt_i32_f32_sdwa v38, v38 dst_sel:WORD_1 dst_unused:UNUSED_PAD src0_sel:DWORD
	v_cvt_i32_f32_e32 v39, v39
	v_lshlrev_b32_e32 v37, 8, v37
	v_and_b32_e32 v37, 0xff00, v37
	v_and_b32_e32 v38, 0xff0000, v38
	v_perm_b32 v36, v39, v36, s65
	v_or3_b32 v36, v36, v37, v38
	v_and_b32_e32 v38, 0xffff0000, v41
	v_and_b32_e32 v37, 0xffff0000, v40
	v_mul_f32_e32 v38, v4, v38
	v_and_b32_e32 v39, 0xffff0000, v42
	v_and_b32_e32 v40, 0xffff0000, v43
	v_mul_f32_e32 v37, v4, v37
	v_rndne_f32_e32 v38, v38
	v_mul_f32_e32 v39, v4, v39
	v_mul_f32_e32 v40, v4, v40
	v_rndne_f32_e32 v37, v37
	v_cvt_i32_f32_e32 v38, v38
	v_rndne_f32_e32 v39, v39
	v_rndne_f32_e32 v40, v40
	v_cvt_i32_f32_e32 v37, v37
	v_cvt_i32_f32_sdwa v39, v39 dst_sel:WORD_1 dst_unused:UNUSED_PAD src0_sel:DWORD
	v_cvt_i32_f32_e32 v40, v40
	v_lshlrev_b32_e32 v38, 8, v38
	v_and_b32_e32 v38, 0xff00, v38
	v_and_b32_e32 v39, 0xff0000, v39
	v_perm_b32 v37, v40, v37, s65
	v_or3_b32 v37, v37, v38, v39
	v_lshlrev_b32_e32 v39, 16, v33
	v_and_b32_e32 v33, 0xffff0000, v33
	v_lshlrev_b32_e32 v38, 16, v32
	v_lshlrev_b32_e32 v40, 16, v34
	v_lshlrev_b32_e32 v41, 16, v35
	v_and_b32_e32 v32, 0xffff0000, v32
	v_mul_f32_e32 v33, v2, v33
	v_and_b32_e32 v34, 0xffff0000, v34
	v_and_b32_e32 v35, 0xffff0000, v35
	v_mul_f32_e32 v39, v3, v39
	v_mul_f32_e32 v32, v2, v32
	v_rndne_f32_e32 v33, v33
	v_mul_f32_e32 v34, v2, v34
	v_mul_f32_e32 v35, v2, v35
	v_mul_f32_e32 v38, v3, v38
	v_rndne_f32_e32 v39, v39
	v_mul_f32_e32 v40, v3, v40
	v_mul_f32_e32 v41, v3, v41
	v_rndne_f32_e32 v32, v32
	v_cvt_i32_f32_e32 v33, v33
	v_rndne_f32_e32 v34, v34
	v_rndne_f32_e32 v35, v35
	v_rndne_f32_e32 v38, v38
	v_cvt_i32_f32_e32 v39, v39
	v_rndne_f32_e32 v40, v40
	v_rndne_f32_e32 v41, v41
	v_cvt_i32_f32_e32 v32, v32
	v_cvt_i32_f32_sdwa v34, v34 dst_sel:WORD_1 dst_unused:UNUSED_PAD src0_sel:DWORD
	v_cvt_i32_f32_e32 v35, v35
	v_cvt_i32_f32_e32 v38, v38
	v_cvt_i32_f32_sdwa v40, v40 dst_sel:WORD_1 dst_unused:UNUSED_PAD src0_sel:DWORD
	v_cvt_i32_f32_e32 v41, v41
	v_lshlrev_b32_e32 v33, 8, v33
	v_lshlrev_b32_e32 v39, 8, v39
	v_and_b32_e32 v33, 0xff00, v33
	v_and_b32_e32 v34, 0xff0000, v34
	v_perm_b32 v32, v35, v32, s65
	v_and_b32_e32 v39, 0xff00, v39
	v_and_b32_e32 v40, 0xff0000, v40
	v_perm_b32 v38, v41, v38, s65
	v_or3_b32 v32, v32, v33, v34
	v_lshlrev_b32_e32 v34, 16, v29
	v_and_b32_e32 v29, 0xffff0000, v29
	v_or3_b32 v38, v38, v39, v40
	v_lshlrev_b32_e32 v33, 16, v28
	v_lshlrev_b32_e32 v35, 16, v30
	v_lshlrev_b32_e32 v39, 16, v31
	v_and_b32_e32 v28, 0xffff0000, v28
	v_mul_f32_e32 v29, v4, v29
	v_and_b32_e32 v30, 0xffff0000, v30
	v_and_b32_e32 v31, 0xffff0000, v31
	v_mul_f32_e32 v28, v4, v28
	v_rndne_f32_e32 v29, v29
	v_mul_f32_e32 v30, v4, v30
	v_mul_f32_e32 v31, v4, v31
	v_rndne_f32_e32 v28, v28
	v_cvt_i32_f32_e32 v29, v29
	v_rndne_f32_e32 v30, v30
	v_rndne_f32_e32 v31, v31
	v_cvt_i32_f32_e32 v28, v28
	v_cvt_i32_f32_sdwa v30, v30 dst_sel:WORD_1 dst_unused:UNUSED_PAD src0_sel:DWORD
	v_cvt_i32_f32_e32 v31, v31
	v_lshlrev_b32_e32 v29, 8, v29
	v_and_b32_e32 v29, 0xff00, v29
	v_and_b32_e32 v30, 0xff0000, v30
	v_perm_b32 v28, v31, v28, s65
	v_or3_b32 v28, v28, v29, v30
	v_lshlrev_b32_e32 v29, 16, v25
	v_and_b32_e32 v25, 0xffff0000, v25
	ds_write2st64_b32 v57, v37, v28 offset0:12 offset1:13
	v_lshlrev_b32_e32 v28, 16, v24
	v_lshlrev_b32_e32 v30, 16, v26
	v_lshlrev_b32_e32 v31, 16, v27
	v_and_b32_e32 v24, 0xffff0000, v24
	v_mul_f32_e32 v25, v2, v25
	v_and_b32_e32 v26, 0xffff0000, v26
	v_and_b32_e32 v27, 0xffff0000, v27
	v_mul_f32_e32 v24, v2, v24
	v_rndne_f32_e32 v25, v25
	v_mul_f32_e32 v26, v2, v26
	v_mul_f32_e32 v27, v2, v27
	v_rndne_f32_e32 v24, v24
	v_cvt_i32_f32_e32 v25, v25
	v_rndne_f32_e32 v26, v26
	v_rndne_f32_e32 v27, v27
	v_cvt_i32_f32_e32 v24, v24
	v_cvt_i32_f32_sdwa v26, v26 dst_sel:WORD_1 dst_unused:UNUSED_PAD src0_sel:DWORD
	v_cvt_i32_f32_e32 v27, v27
	v_lshlrev_b32_e32 v25, 8, v25
	v_and_b32_e32 v25, 0xff00, v25
	v_and_b32_e32 v26, 0xff0000, v26
	v_perm_b32 v24, v27, v24, s65
	v_or3_b32 v24, v24, v25, v26
	v_lshlrev_b32_e32 v25, 16, v21
	v_and_b32_e32 v21, 0xffff0000, v21
	ds_write2st64_b32 v53, v32, v24 offset0:28 offset1:29
	v_lshlrev_b32_e32 v24, 16, v20
	v_lshlrev_b32_e32 v26, 16, v22
	v_lshlrev_b32_e32 v27, 16, v23
	v_and_b32_e32 v20, 0xffff0000, v20
	v_mul_f32_e32 v21, v4, v21
	v_and_b32_e32 v22, 0xffff0000, v22
	v_and_b32_e32 v23, 0xffff0000, v23
	v_mul_f32_e32 v25, v50, v25
	v_mul_f32_e32 v20, v4, v20
	v_rndne_f32_e32 v21, v21
	v_mul_f32_e32 v22, v4, v22
	v_mul_f32_e32 v23, v4, v23
	v_mul_f32_e32 v24, v50, v24
	v_rndne_f32_e32 v25, v25
	v_mul_f32_e32 v26, v50, v26
	v_mul_f32_e32 v27, v50, v27
	v_rndne_f32_e32 v20, v20
	v_cvt_i32_f32_e32 v21, v21
	v_rndne_f32_e32 v22, v22
	v_rndne_f32_e32 v23, v23
	v_rndne_f32_e32 v24, v24
	v_cvt_i32_f32_e32 v25, v25
	v_rndne_f32_e32 v26, v26
	v_rndne_f32_e32 v27, v27
	v_cvt_i32_f32_e32 v20, v20
	v_cvt_i32_f32_sdwa v22, v22 dst_sel:WORD_1 dst_unused:UNUSED_PAD src0_sel:DWORD
	v_cvt_i32_f32_e32 v23, v23
	v_cvt_i32_f32_e32 v24, v24
	v_cvt_i32_f32_sdwa v26, v26 dst_sel:WORD_1 dst_unused:UNUSED_PAD src0_sel:DWORD
	v_cvt_i32_f32_e32 v27, v27
	v_lshlrev_b32_e32 v21, 8, v21
	v_lshlrev_b32_e32 v25, 8, v25
	v_and_b32_e32 v21, 0xff00, v21
	v_and_b32_e32 v22, 0xff0000, v22
	v_perm_b32 v20, v23, v20, s65
	v_and_b32_e32 v25, 0xff00, v25
	v_and_b32_e32 v26, 0xff0000, v26
	v_perm_b32 v24, v27, v24, s65
	v_or3_b32 v20, v20, v21, v22
	v_lshlrev_b32_e32 v22, 16, v17
	v_and_b32_e32 v17, 0xffff0000, v17
	v_or3_b32 v24, v24, v25, v26
	v_lshlrev_b32_e32 v21, 16, v16
	v_lshlrev_b32_e32 v23, 16, v18
	v_lshlrev_b32_e32 v25, 16, v19
	v_and_b32_e32 v16, 0xffff0000, v16
	v_mul_f32_e32 v17, v2, v17
	v_and_b32_e32 v18, 0xffff0000, v18
	v_and_b32_e32 v19, 0xffff0000, v19
	v_mul_f32_e32 v22, v3, v22
	v_mul_f32_e32 v16, v2, v16
	v_rndne_f32_e32 v17, v17
	v_mul_f32_e32 v18, v2, v18
	v_mul_f32_e32 v19, v2, v19
	v_mul_f32_e32 v21, v3, v21
	v_rndne_f32_e32 v22, v22
	v_mul_f32_e32 v23, v3, v23
	v_mul_f32_e32 v25, v3, v25
	v_rndne_f32_e32 v16, v16
	v_cvt_i32_f32_e32 v17, v17
	v_rndne_f32_e32 v18, v18
	v_rndne_f32_e32 v19, v19
	v_rndne_f32_e32 v21, v21
	v_cvt_i32_f32_e32 v22, v22
	v_rndne_f32_e32 v23, v23
	v_rndne_f32_e32 v25, v25
	v_cvt_i32_f32_e32 v16, v16
	v_cvt_i32_f32_sdwa v18, v18 dst_sel:WORD_1 dst_unused:UNUSED_PAD src0_sel:DWORD
	v_cvt_i32_f32_e32 v19, v19
	v_cvt_i32_f32_e32 v21, v21
	v_cvt_i32_f32_sdwa v23, v23 dst_sel:WORD_1 dst_unused:UNUSED_PAD src0_sel:DWORD
	v_cvt_i32_f32_e32 v25, v25
	v_lshlrev_b32_e32 v17, 8, v17
	v_lshlrev_b32_e32 v22, 8, v22
	v_and_b32_e32 v17, 0xff00, v17
	v_and_b32_e32 v18, 0xff0000, v18
	v_perm_b32 v16, v19, v16, s65
	v_and_b32_e32 v22, 0xff00, v22
	v_and_b32_e32 v23, 0xff0000, v23
	v_perm_b32 v21, v25, v21, s65
	v_or3_b32 v16, v16, v17, v18
	v_lshlrev_b32_e32 v18, 16, v13
	v_mul_f32_e32 v51, v50, v51
	v_mul_f32_e32 v34, v50, v34
	v_or3_b32 v21, v21, v22, v23
	v_lshlrev_b32_e32 v17, 16, v12
	v_mul_f32_e32 v18, v50, v18
	v_lshlrev_b32_e32 v19, 16, v14
	v_lshlrev_b32_e32 v22, 16, v15
	v_mul_f32_e32 v49, v50, v49
	v_rndne_f32_e32 v51, v51
	v_mul_f32_e32 v52, v50, v52
	v_mul_f32_e32 v59, v50, v59
	v_mul_f32_e32 v33, v50, v33
	v_rndne_f32_e32 v34, v34
	v_mul_f32_e32 v35, v50, v35
	v_mul_f32_e32 v39, v50, v39
	v_mul_f32_e32 v17, v50, v17
	v_rndne_f32_e32 v18, v18
	v_mul_f32_e32 v19, v50, v19
	v_mul_f32_e32 v22, v50, v22
	v_rndne_f32_e32 v49, v49
	v_cvt_i32_f32_e32 v51, v51
	v_rndne_f32_e32 v52, v52
	v_rndne_f32_e32 v59, v59
	v_rndne_f32_e32 v33, v33
	v_cvt_i32_f32_e32 v34, v34
	v_rndne_f32_e32 v35, v35
	v_rndne_f32_e32 v39, v39
	v_rndne_f32_e32 v17, v17
	v_cvt_i32_f32_e32 v18, v18
	v_rndne_f32_e32 v19, v19
	v_rndne_f32_e32 v22, v22
	v_cvt_i32_f32_e32 v49, v49
	v_cvt_i32_f32_sdwa v52, v52 dst_sel:WORD_1 dst_unused:UNUSED_PAD src0_sel:DWORD
	v_cvt_i32_f32_e32 v59, v59
	v_cvt_i32_f32_e32 v33, v33
	v_cvt_i32_f32_sdwa v35, v35 dst_sel:WORD_1 dst_unused:UNUSED_PAD src0_sel:DWORD
	v_cvt_i32_f32_e32 v39, v39
	v_cvt_i32_f32_e32 v17, v17
	v_cvt_i32_f32_sdwa v19, v19 dst_sel:WORD_1 dst_unused:UNUSED_PAD src0_sel:DWORD
	v_cvt_i32_f32_e32 v22, v22
	v_lshlrev_b32_e32 v51, 8, v51
	v_lshlrev_b32_e32 v34, 8, v34
	v_lshlrev_b32_e32 v18, 8, v18
	v_and_b32_e32 v51, 0xff00, v51
	v_and_b32_e32 v52, 0xff0000, v52
	v_perm_b32 v49, v59, v49, s65
	v_and_b32_e32 v34, 0xff00, v34
	v_and_b32_e32 v35, 0xff0000, v35
	v_perm_b32 v33, v39, v33, s65
	v_and_b32_e32 v18, 0xff00, v18
	v_and_b32_e32 v19, 0xff0000, v19
	v_perm_b32 v17, v22, v17, s65
	v_or3_b32 v49, v49, v51, v52
	v_or3_b32 v33, v33, v34, v35
	v_or3_b32 v17, v17, v18, v19
	ds_write2st64_b32 v5, v54, v49 offset0:2 offset1:3
	ds_write2st64_b32 v5, v36, v33 offset0:4 offset1:5
	ds_write2st64_b32 v5, v24, v17 offset0:6 offset1:7
	v_and_b32_e32 v5, 0xffff0000, v12
	v_and_b32_e32 v12, 0xffff0000, v13
	v_mul_f32_e32 v12, v4, v12
	v_and_b32_e32 v13, 0xffff0000, v14
	v_and_b32_e32 v14, 0xffff0000, v15
	v_mul_f32_e32 v5, v4, v5
	v_rndne_f32_e32 v12, v12
	v_mul_f32_e32 v13, v4, v13
	v_mul_f32_e32 v4, v4, v14
	v_rndne_f32_e32 v5, v5
	v_cvt_i32_f32_e32 v12, v12
	v_rndne_f32_e32 v13, v13
	v_rndne_f32_e32 v4, v4
	v_cvt_i32_f32_e32 v5, v5
	v_cvt_i32_f32_sdwa v13, v13 dst_sel:WORD_1 dst_unused:UNUSED_PAD src0_sel:DWORD
	v_cvt_i32_f32_e32 v4, v4
	v_lshlrev_b32_e32 v12, 8, v12
	v_and_b32_e32 v12, 0xff00, v12
	v_and_b32_e32 v13, 0xff0000, v13
	v_perm_b32 v4, v4, v5, s65
	v_or3_b32 v4, v4, v12, v13
	v_lshlrev_b32_e32 v5, 16, v8
	ds_write2st64_b32 v57, v20, v4 offset0:14 offset1:15
	v_lshlrev_b32_e32 v4, 16, v7
	v_mul_f32_e32 v5, v3, v5
	v_lshlrev_b32_e32 v12, 16, v9
	v_lshlrev_b32_e32 v13, 16, v10
	v_mul_f32_e32 v44, v3, v44
	v_mul_f32_e32 v45, v3, v45
	v_mul_f32_e32 v46, v3, v46
	v_mul_f32_e32 v47, v3, v47
	v_mul_f32_e32 v28, v3, v28
	v_mul_f32_e32 v29, v3, v29
	v_mul_f32_e32 v30, v3, v30
	v_mul_f32_e32 v31, v3, v31
	v_mul_f32_e32 v4, v3, v4
	v_rndne_f32_e32 v5, v5
	v_mul_f32_e32 v12, v3, v12
	v_mul_f32_e32 v3, v3, v13
	v_rndne_f32_e32 v4, v4
	v_cvt_i32_f32_e32 v5, v5
	v_rndne_f32_e32 v12, v12
	v_rndne_f32_e32 v3, v3
	v_cvt_i32_f32_e32 v4, v4
	v_cvt_i32_f32_sdwa v12, v12 dst_sel:WORD_1 dst_unused:UNUSED_PAD src0_sel:DWORD
	v_cvt_i32_f32_e32 v3, v3
	v_lshlrev_b32_e32 v5, 8, v5
	v_and_b32_e32 v5, 0xff00, v5
	v_and_b32_e32 v12, 0xff0000, v12
	v_perm_b32 v3, v3, v4, s65
	v_or3_b32 v3, v3, v5, v12
	v_and_b32_e32 v4, 0xffff0000, v8
	ds_write2st64_b32 v58, v21, v3 offset0:22 offset1:23
	v_and_b32_e32 v3, 0xffff0000, v7
	v_mul_f32_e32 v4, v2, v4
	v_and_b32_e32 v5, 0xffff0000, v9
	v_and_b32_e32 v7, 0xffff0000, v10
	v_rndne_f32_e32 v45, v45
	v_rndne_f32_e32 v29, v29
	v_mul_f32_e32 v3, v2, v3
	v_rndne_f32_e32 v4, v4
	v_mul_f32_e32 v5, v2, v5
	v_mul_f32_e32 v2, v2, v7
	v_rndne_f32_e32 v44, v44
	v_cvt_i32_f32_e32 v45, v45
	v_rndne_f32_e32 v46, v46
	v_rndne_f32_e32 v47, v47
	v_rndne_f32_e32 v28, v28
	v_cvt_i32_f32_e32 v29, v29
	v_rndne_f32_e32 v30, v30
	v_rndne_f32_e32 v31, v31
	v_rndne_f32_e32 v3, v3
	v_cvt_i32_f32_e32 v4, v4
	v_rndne_f32_e32 v5, v5
	v_rndne_f32_e32 v2, v2
	v_cvt_i32_f32_e32 v44, v44
	v_cvt_i32_f32_sdwa v46, v46 dst_sel:WORD_1 dst_unused:UNUSED_PAD src0_sel:DWORD
	v_cvt_i32_f32_e32 v47, v47
	v_cvt_i32_f32_e32 v28, v28
	v_cvt_i32_f32_sdwa v30, v30 dst_sel:WORD_1 dst_unused:UNUSED_PAD src0_sel:DWORD
	v_cvt_i32_f32_e32 v31, v31
	v_cvt_i32_f32_e32 v3, v3
	v_cvt_i32_f32_sdwa v5, v5 dst_sel:WORD_1 dst_unused:UNUSED_PAD src0_sel:DWORD
	v_cvt_i32_f32_e32 v2, v2
	v_lshlrev_b32_e32 v45, 8, v45
	v_lshlrev_b32_e32 v29, 8, v29
	v_lshlrev_b32_e32 v4, 8, v4
	v_and_b32_e32 v45, 0xff00, v45
	v_and_b32_e32 v46, 0xff0000, v46
	v_perm_b32 v44, v47, v44, s65
	v_and_b32_e32 v29, 0xff00, v29
	v_and_b32_e32 v30, 0xff0000, v30
	v_perm_b32 v28, v31, v28, s65
	v_and_b32_e32 v4, 0xff00, v4
	v_and_b32_e32 v5, 0xff0000, v5
	v_perm_b32 v2, v2, v3, s65
	v_or3_b32 v44, v44, v45, v46
	v_or3_b32 v28, v28, v29, v30
	v_or3_b32 v2, v2, v4, v5
	ds_write2st64_b32 v58, v56, v44 offset0:18 offset1:19
	ds_write2st64_b32 v58, v38, v28 offset0:20 offset1:21
	ds_write2st64_b32 v53, v16, v2 offset0:30 offset1:31
	s_waitcnt lgkmcnt(0)
	s_barrier
	v_cmp_eq_u32_e32 vcc, 0, v0
	s_and_saveexec_b64 s[98:99], vcc
	v_mov_b32_e32 v200, 1
	s_nop 0
	global_atomic_add v200, v11, v200, s[16:17] sc0
	s_mov_b64 exec, s[98:99]
	v_cmp_gt_i32_e32 vcc, s66, v6
	s_and_saveexec_b64 s[8:9], vcc
	s_cbranch_execz .LBB0_238
	s_and_b64 s[4:5], s[4:5], exec
	s_cselect_b32 s10, 0x80, 0
	v_lshlrev_b32_e32 v2, 4, v6
	s_mov_b64 s[4:5], 0

.LBB0_249:
	s_or_b64 exec, exec, s[4:5]
	s_nop 0
	v_max_f32_e32 v2, v2, v2
	v_max_f32_e32 v2, 0xda24260, v2
	v_div_scale_f32 v8, s[4:5], v2, v2, s63
	v_rcp_f32_e32 v9, v8
	v_div_scale_f32 v116, vcc, s63, v2, s63
	v_max_f32_e32 v3, v3, v3
	v_fma_f32 v117, -v8, v9, 1.0
	v_fmac_f32_e32 v9, v117, v9
	v_mul_f32_e32 v117, v116, v9
	v_fma_f32 v118, -v8, v117, v116
	v_fmac_f32_e32 v117, v118, v9
	v_max_f32_e32 v3, 0xda24260, v3
	v_fma_f32 v8, -v8, v117, v116
	v_div_scale_f32 v116, s[4:5], v3, v3, s63
	v_rcp_f32_e32 v118, v116
	v_div_fmas_f32 v8, v8, v9, v117
	v_div_fixup_f32 v8, v8, v2, s63
	v_max_f32_e32 v4, v4, v4
	v_fma_f32 v2, -v116, v118, 1.0
	v_fmac_f32_e32 v118, v2, v118
	v_div_scale_f32 v2, vcc, s63, v3, s63
	v_mul_f32_e32 v9, v2, v118
	v_fma_f32 v117, -v116, v9, v2
	v_fmac_f32_e32 v9, v117, v118
	v_fma_f32 v2, -v116, v9, v2
	v_max_f32_e32 v116, 0xda24260, v4
	v_div_scale_f32 v117, s[4:5], v116, v116, s63
	v_rcp_f32_e32 v119, v117
	v_div_fmas_f32 v2, v2, v118, v9
	v_div_fixup_f32 v4, v2, v3, s63
	v_max_f32_e32 v5, v5, v5
	v_fma_f32 v2, -v117, v119, 1.0
	v_fmac_f32_e32 v119, v2, v119
	v_div_scale_f32 v2, vcc, s63, v116, s63
	v_mul_f32_e32 v3, v2, v119
	v_fma_f32 v9, -v117, v3, v2
	v_max_f32_e32 v5, 0xda24260, v5
	v_fmac_f32_e32 v3, v9, v119
	v_div_scale_f32 v9, s[4:5], v5, v5, s63
	v_fma_f32 v2, -v117, v3, v2
	v_rcp_f32_e32 v117, v9
	v_div_fmas_f32 v2, v2, v119, v3
	v_div_fixup_f32 v3, v2, v116, s63
	s_movk_i32 s4, 0x5840
	v_fma_f32 v2, -v9, v117, 1.0
	v_fmac_f32_e32 v117, v2, v117
	v_div_scale_f32 v2, vcc, s63, v5, s63
	v_mul_f32_e32 v116, v2, v117
	v_fma_f32 v118, -v9, v116, v2
	v_fmac_f32_e32 v116, v118, v117
	v_fma_f32 v2, -v9, v116, v2
	v_div_fmas_f32 v2, v2, v117, v116
	v_div_fixup_f32 v2, v2, v5, s63
	v_mul_lo_u32 v5, v99, s4
	v_lshlrev_b32_e32 v9, 16, v113
	v_add3_u32 v5, 0, v5, v6
	v_lshlrev_b32_e32 v6, 16, v112
	v_mul_f32_e32 v9, v8, v9
	v_lshlrev_b32_e32 v99, 16, v114
	v_lshlrev_b32_e32 v116, 16, v115
	v_mul_f32_e32 v6, v8, v6
	v_rndne_f32_e32 v9, v9
	v_mul_f32_e32 v99, v8, v99
	v_mul_f32_e32 v116, v8, v116
	v_rndne_f32_e32 v6, v6
	v_cvt_i32_f32_e32 v9, v9
	v_rndne_f32_e32 v99, v99
	v_rndne_f32_e32 v116, v116
	v_cvt_i32_f32_e32 v6, v6
	v_cvt_i32_f32_sdwa v99, v99 dst_sel:WORD_1 dst_unused:UNUSED_PAD src0_sel:DWORD
	v_cvt_i32_f32_e32 v116, v116
	v_lshlrev_b32_e32 v9, 8, v9
	v_and_b32_e32 v9, 0xff00, v9
	v_and_b32_e32 v99, 0xff0000, v99
	v_perm_b32 v6, v116, v6, s65
	v_or3_b32 v99, v6, v9, v99
	v_and_b32_e32 v9, 0xffff0000, v113
	v_and_b32_e32 v6, 0xffff0000, v112
	v_mul_f32_e32 v9, v4, v9
	v_and_b32_e32 v112, 0xffff0000, v114
	v_and_b32_e32 v113, 0xffff0000, v115
	v_mul_f32_e32 v6, v4, v6
	v_rndne_f32_e32 v9, v9
	v_mul_f32_e32 v112, v4, v112
	v_mul_f32_e32 v113, v4, v113
	v_rndne_f32_e32 v6, v6
	v_cvt_i32_f32_e32 v9, v9
	v_rndne_f32_e32 v112, v112
	v_rndne_f32_e32 v113, v113
	v_cvt_i32_f32_e32 v6, v6
	v_cvt_i32_f32_sdwa v112, v112 dst_sel:WORD_1 dst_unused:UNUSED_PAD src0_sel:DWORD
	v_cvt_i32_f32_e32 v113, v113
	v_lshlrev_b32_e32 v9, 8, v9
	v_and_b32_e32 v9, 0xff00, v9
	v_and_b32_e32 v112, 0xff0000, v112
	v_perm_b32 v6, v113, v6, s65
	v_or3_b32 v9, v6, v9, v112
	v_lshlrev_b32_e32 v112, 16, v109
	v_lshlrev_b32_e32 v6, 16, v108
	v_mul_f32_e32 v112, v3, v112
	v_lshlrev_b32_e32 v113, 16, v110
	v_lshlrev_b32_e32 v114, 16, v111
	v_mul_f32_e32 v6, v3, v6
	v_rndne_f32_e32 v112, v112
	v_mul_f32_e32 v113, v3, v113
	v_mul_f32_e32 v114, v3, v114
	v_rndne_f32_e32 v6, v6
	v_cvt_i32_f32_e32 v112, v112
	v_rndne_f32_e32 v113, v113
	v_rndne_f32_e32 v114, v114
	v_cvt_i32_f32_e32 v6, v6
	v_cvt_i32_f32_sdwa v113, v113 dst_sel:WORD_1 dst_unused:UNUSED_PAD src0_sel:DWORD
	v_cvt_i32_f32_e32 v114, v114
	v_lshlrev_b32_e32 v112, 8, v112
	v_and_b32_e32 v112, 0xff00, v112
	v_and_b32_e32 v113, 0xff0000, v113
	v_perm_b32 v6, v114, v6, s65
	v_or3_b32 v112, v6, v112, v113
	v_and_b32_e32 v6, 0xffff0000, v108
	v_and_b32_e32 v108, 0xffff0000, v109
	v_mul_f32_e32 v108, v2, v108
	v_and_b32_e32 v109, 0xffff0000, v110
	v_and_b32_e32 v110, 0xffff0000, v111
	v_mul_f32_e32 v6, v2, v6
	v_rndne_f32_e32 v108, v108
	v_mul_f32_e32 v109, v2, v109
	v_mul_f32_e32 v110, v2, v110
	v_rndne_f32_e32 v6, v6
	v_cvt_i32_f32_e32 v108, v108
	v_rndne_f32_e32 v109, v109
	v_rndne_f32_e32 v110, v110
	v_cvt_i32_f32_e32 v6, v6
	v_cvt_i32_f32_sdwa v109, v109 dst_sel:WORD_1 dst_unused:UNUSED_PAD src0_sel:DWORD
	v_cvt_i32_f32_e32 v110, v110
	v_lshlrev_b32_e32 v108, 8, v108
	v_and_b32_e32 v108, 0xff00, v108
	v_and_b32_e32 v109, 0xff0000, v109
	v_perm_b32 v6, v110, v6, s65
	v_or3_b32 v6, v6, v108, v109
	v_lshlrev_b32_e32 v109, 16, v105
	v_lshlrev_b32_e32 v108, 16, v104
	v_mul_f32_e32 v109, v8, v109
	v_lshlrev_b32_e32 v110, 16, v106
	v_lshlrev_b32_e32 v111, 16, v107
	v_mul_f32_e32 v108, v8, v108
	v_rndne_f32_e32 v109, v109
	v_mul_f32_e32 v110, v8, v110
	v_mul_f32_e32 v111, v8, v111
	v_rndne_f32_e32 v108, v108
	v_cvt_i32_f32_e32 v109, v109
	v_rndne_f32_e32 v110, v110
	v_rndne_f32_e32 v111, v111
	v_cvt_i32_f32_e32 v108, v108
	v_cvt_i32_f32_sdwa v110, v110 dst_sel:WORD_1 dst_unused:UNUSED_PAD src0_sel:DWORD
	v_cvt_i32_f32_e32 v111, v111
	v_lshlrev_b32_e32 v109, 8, v109
	v_and_b32_e32 v109, 0xff00, v109
	v_and_b32_e32 v110, 0xff0000, v110
	v_perm_b32 v108, v111, v108, s65
	v_or3_b32 v108, v108, v109, v110
	ds_write2st64_b32 v5, v99, v108 offset1:2
	v_and_b32_e32 v99, 0xffff0000, v104
	v_and_b32_e32 v104, 0xffff0000, v105
	v_mul_f32_e32 v104, v4, v104
	v_and_b32_e32 v105, 0xffff0000, v106
	v_and_b32_e32 v106, 0xffff0000, v107
	v_mul_f32_e32 v99, v4, v99
	v_rndne_f32_e32 v104, v104
	v_mul_f32_e32 v105, v4, v105
	v_mul_f32_e32 v106, v4, v106
	v_rndne_f32_e32 v99, v99
	v_cvt_i32_f32_e32 v104, v104
	v_rndne_f32_e32 v105, v105
	v_rndne_f32_e32 v106, v106
	v_cvt_i32_f32_e32 v99, v99
	v_cvt_i32_f32_sdwa v105, v105 dst_sel:WORD_1 dst_unused:UNUSED_PAD src0_sel:DWORD
	v_cvt_i32_f32_e32 v106, v106
	v_lshlrev_b32_e32 v104, 8, v104
	v_and_b32_e32 v104, 0xff00, v104
	v_and_b32_e32 v105, 0xff0000, v105
	v_perm_b32 v99, v106, v99, s65
	v_or3_b32 v104, v99, v104, v105
	v_lshlrev_b32_e32 v105, 16, v96
	v_and_b32_e32 v96, 0xffff0000, v96
	v_lshlrev_b32_e32 v99, 16, v95
	v_mul_f32_e32 v105, v3, v105
	v_lshlrev_b32_e32 v106, 16, v97
	v_lshlrev_b32_e32 v107, 16, v98
	v_and_b32_e32 v95, 0xffff0000, v95
	v_mul_f32_e32 v96, v2, v96
	v_and_b32_e32 v97, 0xffff0000, v97
	v_and_b32_e32 v98, 0xffff0000, v98
	v_mul_f32_e32 v99, v3, v99
	v_rndne_f32_e32 v105, v105
	v_mul_f32_e32 v106, v3, v106
	v_mul_f32_e32 v107, v3, v107
	v_mul_f32_e32 v95, v2, v95
	v_rndne_f32_e32 v96, v96
	v_mul_f32_e32 v97, v2, v97
	v_mul_f32_e32 v98, v2, v98
	v_rndne_f32_e32 v99, v99
	v_cvt_i32_f32_e32 v105, v105
	v_rndne_f32_e32 v106, v106
	v_rndne_f32_e32 v107, v107
	v_rndne_f32_e32 v95, v95
	v_cvt_i32_f32_e32 v96, v96
	v_rndne_f32_e32 v97, v97
	v_rndne_f32_e32 v98, v98
	v_cvt_i32_f32_e32 v99, v99
	v_cvt_i32_f32_sdwa v106, v106 dst_sel:WORD_1 dst_unused:UNUSED_PAD src0_sel:DWORD
	v_cvt_i32_f32_e32 v107, v107
	v_cvt_i32_f32_e32 v95, v95
	v_cvt_i32_f32_sdwa v97, v97 dst_sel:WORD_1 dst_unused:UNUSED_PAD src0_sel:DWORD
	v_cvt_i32_f32_e32 v98, v98
	v_lshlrev_b32_e32 v105, 8, v105
	v_lshlrev_b32_e32 v96, 8, v96
	v_and_b32_e32 v105, 0xff00, v105
	v_and_b32_e32 v106, 0xff0000, v106
	v_perm_b32 v99, v107, v99, s65
	v_and_b32_e32 v96, 0xff00, v96
	v_and_b32_e32 v97, 0xff0000, v97
	v_perm_b32 v95, v98, v95, s65
	v_or3_b32 v105, v99, v105, v106
	v_add_u32_e32 v99, 32, v5
	v_or3_b32 v96, v95, v96, v97
	v_lshlrev_b32_e32 v97, 16, v101
	ds_write2st64_b32 v99, v112, v105 offset0:44 offset1:46
	v_lshlrev_b32_e32 v95, 16, v100
	v_mul_f32_e32 v97, v8, v97
	v_lshlrev_b32_e32 v98, 16, v102
	v_lshlrev_b32_e32 v105, 16, v103
	v_mul_f32_e32 v95, v8, v95
	v_rndne_f32_e32 v97, v97
	v_mul_f32_e32 v98, v8, v98
	v_mul_f32_e32 v105, v8, v105
	v_rndne_f32_e32 v95, v95
	v_cvt_i32_f32_e32 v97, v97
	v_rndne_f32_e32 v98, v98
	v_rndne_f32_e32 v105, v105
	v_cvt_i32_f32_e32 v95, v95
	v_cvt_i32_f32_sdwa v98, v98 dst_sel:WORD_1 dst_unused:UNUSED_PAD src0_sel:DWORD
	v_cvt_i32_f32_e32 v105, v105
	v_lshlrev_b32_e32 v97, 8, v97
	v_and_b32_e32 v97, 0xff00, v97
	v_and_b32_e32 v98, 0xff0000, v98
	v_perm_b32 v95, v105, v95, s65
	v_or3_b32 v97, v95, v97, v98
	v_and_b32_e32 v98, 0xffff0000, v101
	v_and_b32_e32 v95, 0xffff0000, v100
	v_mul_f32_e32 v98, v4, v98
	v_and_b32_e32 v100, 0xffff0000, v102
	v_and_b32_e32 v101, 0xffff0000, v103
	v_mul_f32_e32 v95, v4, v95
	v_rndne_f32_e32 v98, v98
	v_mul_f32_e32 v100, v4, v100
	v_mul_f32_e32 v101, v4, v101
	v_rndne_f32_e32 v95, v95
	v_cvt_i32_f32_e32 v98, v98
	v_rndne_f32_e32 v100, v100
	v_rndne_f32_e32 v101, v101
	v_cvt_i32_f32_e32 v95, v95
	v_cvt_i32_f32_sdwa v100, v100 dst_sel:WORD_1 dst_unused:UNUSED_PAD src0_sel:DWORD
	v_cvt_i32_f32_e32 v101, v101
	v_lshlrev_b32_e32 v98, 8, v98
	v_and_b32_e32 v98, 0xff00, v98
	v_and_b32_e32 v100, 0xff0000, v100
	v_perm_b32 v95, v101, v95, s65
	v_or3_b32 v98, v95, v98, v100
	v_add_u32_e32 v95, 16, v5
	v_lshlrev_b32_e32 v100, 16, v76
	v_and_b32_e32 v76, 0xffff0000, v76
	ds_write2st64_b32 v95, v104, v98 offset0:24 offset1:26
	v_lshlrev_b32_e32 v98, 16, v75
	v_lshlrev_b32_e32 v101, 16, v77
	v_lshlrev_b32_e32 v102, 16, v94
	v_and_b32_e32 v75, 0xffff0000, v75
	v_mul_f32_e32 v76, v2, v76
	v_and_b32_e32 v77, 0xffff0000, v77
	v_and_b32_e32 v94, 0xffff0000, v94
	v_mul_f32_e32 v75, v2, v75
	v_rndne_f32_e32 v76, v76
	v_mul_f32_e32 v77, v2, v77
	v_mul_f32_e32 v94, v2, v94
	v_rndne_f32_e32 v75, v75
	v_cvt_i32_f32_e32 v76, v76
	v_rndne_f32_e32 v77, v77
	v_rndne_f32_e32 v94, v94
	v_cvt_i32_f32_e32 v75, v75
	v_cvt_i32_f32_sdwa v77, v77 dst_sel:WORD_1 dst_unused:UNUSED_PAD src0_sel:DWORD
	v_cvt_i32_f32_e32 v94, v94
	v_lshlrev_b32_e32 v76, 8, v76
	v_and_b32_e32 v76, 0xff00, v76
	v_and_b32_e32 v77, 0xff0000, v77
	v_perm_b32 v75, v94, v75, s65
	v_or3_b32 v76, v75, v76, v77
	v_add_u32_e32 v75, 48, v5
	v_lshlrev_b32_e32 v77, 16, v72
	v_and_b32_e32 v72, 0xffff0000, v72
	ds_write2st64_b32 v75, v96, v76 offset0:68 offset1:70
	v_lshlrev_b32_e32 v76, 16, v70
	v_mul_f32_e32 v77, v8, v77
	v_lshlrev_b32_e32 v94, 16, v73
	v_lshlrev_b32_e32 v96, 16, v74
	v_and_b32_e32 v70, 0xffff0000, v70
	v_mul_f32_e32 v72, v4, v72
	v_and_b32_e32 v73, 0xffff0000, v73
	v_and_b32_e32 v74, 0xffff0000, v74
	v_mul_f32_e32 v76, v8, v76
	v_rndne_f32_e32 v77, v77
	v_mul_f32_e32 v94, v8, v94
	v_mul_f32_e32 v96, v8, v96
	v_mul_f32_e32 v70, v4, v70
	v_rndne_f32_e32 v72, v72
	v_mul_f32_e32 v73, v4, v73
	v_mul_f32_e32 v74, v4, v74
	v_rndne_f32_e32 v76, v76
	v_cvt_i32_f32_e32 v77, v77
	v_rndne_f32_e32 v94, v94
	v_rndne_f32_e32 v96, v96
	v_rndne_f32_e32 v70, v70
	v_cvt_i32_f32_e32 v72, v72
	v_rndne_f32_e32 v73, v73
	v_rndne_f32_e32 v74, v74
	v_cvt_i32_f32_e32 v76, v76
	v_cvt_i32_f32_sdwa v94, v94 dst_sel:WORD_1 dst_unused:UNUSED_PAD src0_sel:DWORD
	v_cvt_i32_f32_e32 v96, v96
	v_cvt_i32_f32_e32 v70, v70
	v_cvt_i32_f32_sdwa v73, v73 dst_sel:WORD_1 dst_unused:UNUSED_PAD src0_sel:DWORD
	v_cvt_i32_f32_e32 v74, v74
	v_lshlrev_b32_e32 v77, 8, v77
	v_lshlrev_b32_e32 v72, 8, v72
	v_and_b32_e32 v77, 0xff00, v77
	v_and_b32_e32 v94, 0xff0000, v94
	v_perm_b32 v76, v96, v76, s65
	v_and_b32_e32 v72, 0xff00, v72
	v_and_b32_e32 v73, 0xff0000, v73
	v_perm_b32 v70, v74, v70, s65
	v_or3_b32 v76, v76, v77, v94
	v_or3_b32 v70, v70, v72, v73
	v_lshlrev_b32_e32 v73, 16, v64
	v_and_b32_e32 v64, 0xffff0000, v64
	v_mul_f32_e32 v100, v3, v100
	ds_write2st64_b32 v5, v97, v76 offset0:4 offset1:6
	v_lshlrev_b32_e32 v72, 16, v62
	v_mul_f32_e32 v73, v3, v73
	v_lshlrev_b32_e32 v74, 16, v65
	v_lshlrev_b32_e32 v76, 16, v66
	v_and_b32_e32 v62, 0xffff0000, v62
	v_mul_f32_e32 v64, v2, v64
	v_and_b32_e32 v65, 0xffff0000, v65
	v_and_b32_e32 v66, 0xffff0000, v66
	v_mul_f32_e32 v98, v3, v98
	v_rndne_f32_e32 v100, v100
	v_mul_f32_e32 v101, v3, v101
	v_mul_f32_e32 v102, v3, v102
	v_mul_f32_e32 v72, v3, v72
	v_rndne_f32_e32 v73, v73
	v_mul_f32_e32 v74, v3, v74
	v_mul_f32_e32 v76, v3, v76
	v_mul_f32_e32 v62, v2, v62
	v_rndne_f32_e32 v64, v64
	v_mul_f32_e32 v65, v2, v65
	v_mul_f32_e32 v66, v2, v66
	v_rndne_f32_e32 v98, v98
	v_cvt_i32_f32_e32 v100, v100
	v_rndne_f32_e32 v101, v101
	v_rndne_f32_e32 v102, v102
	v_rndne_f32_e32 v72, v72
	v_cvt_i32_f32_e32 v73, v73
	v_rndne_f32_e32 v74, v74
	v_rndne_f32_e32 v76, v76
	v_rndne_f32_e32 v62, v62
	v_cvt_i32_f32_e32 v64, v64
	v_rndne_f32_e32 v65, v65
	v_rndne_f32_e32 v66, v66
	v_cvt_i32_f32_e32 v98, v98
	v_cvt_i32_f32_sdwa v101, v101 dst_sel:WORD_1 dst_unused:UNUSED_PAD src0_sel:DWORD
	v_cvt_i32_f32_e32 v102, v102
	v_cvt_i32_f32_e32 v72, v72
	v_cvt_i32_f32_sdwa v74, v74 dst_sel:WORD_1 dst_unused:UNUSED_PAD src0_sel:DWORD
	v_cvt_i32_f32_e32 v76, v76
	v_cvt_i32_f32_e32 v62, v62
	v_cvt_i32_f32_sdwa v65, v65 dst_sel:WORD_1 dst_unused:UNUSED_PAD src0_sel:DWORD
	v_cvt_i32_f32_e32 v66, v66
	v_lshlrev_b32_e32 v100, 8, v100
	v_lshlrev_b32_e32 v73, 8, v73
	v_lshlrev_b32_e32 v64, 8, v64
	v_and_b32_e32 v100, 0xff00, v100
	v_and_b32_e32 v101, 0xff0000, v101
	v_perm_b32 v98, v102, v98, s65
	v_and_b32_e32 v73, 0xff00, v73
	v_and_b32_e32 v74, 0xff0000, v74
	v_perm_b32 v72, v76, v72, s65
	v_and_b32_e32 v64, 0xff00, v64
	v_and_b32_e32 v65, 0xff0000, v65
	v_perm_b32 v62, v66, v62, s65
	v_or3_b32 v98, v98, v100, v101
	v_or3_b32 v72, v72, v73, v74
	v_or3_b32 v62, v62, v64, v65
	v_lshlrev_b32_e32 v65, 16, v68
	ds_write2st64_b32 v99, v98, v72 offset0:48 offset1:50
	v_lshlrev_b32_e32 v64, 16, v67
	v_mul_f32_e32 v65, v8, v65
	v_lshlrev_b32_e32 v66, 16, v69
	v_lshlrev_b32_e32 v72, 16, v71
	v_mul_f32_e32 v64, v8, v64
	v_rndne_f32_e32 v65, v65
	v_mul_f32_e32 v66, v8, v66
	v_mul_f32_e32 v72, v8, v72
	v_rndne_f32_e32 v64, v64
	v_cvt_i32_f32_e32 v65, v65
	v_rndne_f32_e32 v66, v66
	v_rndne_f32_e32 v72, v72
	v_cvt_i32_f32_e32 v64, v64
	v_cvt_i32_f32_sdwa v66, v66 dst_sel:WORD_1 dst_unused:UNUSED_PAD src0_sel:DWORD
	v_cvt_i32_f32_e32 v72, v72
	v_lshlrev_b32_e32 v65, 8, v65
	v_and_b32_e32 v65, 0xff00, v65
	v_and_b32_e32 v66, 0xff0000, v66
	v_perm_b32 v64, v72, v64, s65
	v_or3_b32 v64, v64, v65, v66
	v_and_b32_e32 v66, 0xffff0000, v68
	v_and_b32_e32 v65, 0xffff0000, v67
	v_mul_f32_e32 v66, v4, v66
	v_and_b32_e32 v67, 0xffff0000, v69
	v_and_b32_e32 v68, 0xffff0000, v71
	v_mul_f32_e32 v65, v4, v65
	v_rndne_f32_e32 v66, v66
	v_mul_f32_e32 v67, v4, v67
	v_mul_f32_e32 v68, v4, v68
	v_rndne_f32_e32 v65, v65
	v_cvt_i32_f32_e32 v66, v66
	v_rndne_f32_e32 v67, v67
	v_rndne_f32_e32 v68, v68
	v_cvt_i32_f32_e32 v65, v65
	v_cvt_i32_f32_sdwa v67, v67 dst_sel:WORD_1 dst_unused:UNUSED_PAD src0_sel:DWORD
	v_cvt_i32_f32_e32 v68, v68
	v_lshlrev_b32_e32 v66, 8, v66
	v_and_b32_e32 v66, 0xff00, v66
	v_and_b32_e32 v67, 0xff0000, v67
	v_perm_b32 v65, v68, v65, s65
	v_or3_b32 v65, v65, v66, v67
	v_lshlrev_b32_e32 v66, 16, v60
	v_and_b32_e32 v60, 0xffff0000, v60
	ds_write2st64_b32 v95, v70, v65 offset0:28 offset1:30
	v_lshlrev_b32_e32 v65, 16, v59
	v_lshlrev_b32_e32 v67, 16, v61
	v_lshlrev_b32_e32 v68, 16, v63
	v_and_b32_e32 v59, 0xffff0000, v59
	v_mul_f32_e32 v60, v2, v60
	v_and_b32_e32 v61, 0xffff0000, v61
	v_and_b32_e32 v63, 0xffff0000, v63
	v_mul_f32_e32 v59, v2, v59
	v_rndne_f32_e32 v60, v60
	v_mul_f32_e32 v61, v2, v61
	v_mul_f32_e32 v63, v2, v63
	v_rndne_f32_e32 v59, v59
	v_cvt_i32_f32_e32 v60, v60
	v_rndne_f32_e32 v61, v61
	v_rndne_f32_e32 v63, v63
	v_cvt_i32_f32_e32 v59, v59
	v_cvt_i32_f32_sdwa v61, v61 dst_sel:WORD_1 dst_unused:UNUSED_PAD src0_sel:DWORD
	v_cvt_i32_f32_e32 v63, v63
	v_lshlrev_b32_e32 v60, 8, v60
	v_and_b32_e32 v60, 0xff00, v60
	v_and_b32_e32 v61, 0xff0000, v61
	v_perm_b32 v59, v63, v59, s65
	v_or3_b32 v59, v59, v60, v61
	v_lshlrev_b32_e32 v60, 16, v56
	v_and_b32_e32 v56, 0xffff0000, v56
	ds_write2st64_b32 v75, v62, v59 offset0:72 offset1:74
	v_lshlrev_b32_e32 v59, 16, v54
	v_mul_f32_e32 v60, v8, v60
	v_lshlrev_b32_e32 v61, 16, v57
	v_lshlrev_b32_e32 v62, 16, v58
	v_and_b32_e32 v54, 0xffff0000, v54
	v_mul_f32_e32 v56, v4, v56
	v_and_b32_e32 v57, 0xffff0000, v57
	v_and_b32_e32 v58, 0xffff0000, v58
	v_mul_f32_e32 v59, v8, v59
	v_rndne_f32_e32 v60, v60
	v_mul_f32_e32 v61, v8, v61
	v_mul_f32_e32 v62, v8, v62
	v_mul_f32_e32 v54, v4, v54
	v_rndne_f32_e32 v56, v56
	v_mul_f32_e32 v57, v4, v57
	v_mul_f32_e32 v58, v4, v58
	v_rndne_f32_e32 v59, v59
	v_cvt_i32_f32_e32 v60, v60
	v_rndne_f32_e32 v61, v61
	v_rndne_f32_e32 v62, v62
	v_rndne_f32_e32 v54, v54
	v_cvt_i32_f32_e32 v56, v56
	v_rndne_f32_e32 v57, v57
	v_rndne_f32_e32 v58, v58
	v_cvt_i32_f32_e32 v59, v59
	v_cvt_i32_f32_sdwa v61, v61 dst_sel:WORD_1 dst_unused:UNUSED_PAD src0_sel:DWORD
	v_cvt_i32_f32_e32 v62, v62
	v_cvt_i32_f32_e32 v54, v54
	v_cvt_i32_f32_sdwa v57, v57 dst_sel:WORD_1 dst_unused:UNUSED_PAD src0_sel:DWORD
	v_cvt_i32_f32_e32 v58, v58
	v_lshlrev_b32_e32 v60, 8, v60
	v_lshlrev_b32_e32 v56, 8, v56
	v_and_b32_e32 v60, 0xff00, v60
	v_and_b32_e32 v61, 0xff0000, v61
	v_perm_b32 v59, v62, v59, s65
	v_and_b32_e32 v56, 0xff00, v56
	v_and_b32_e32 v57, 0xff0000, v57
	v_perm_b32 v54, v58, v54, s65
	v_or3_b32 v59, v59, v60, v61
	v_or3_b32 v54, v54, v56, v57
	v_lshlrev_b32_e32 v57, 16, v48
	v_and_b32_e32 v48, 0xffff0000, v48
	v_mul_f32_e32 v66, v3, v66
	ds_write2st64_b32 v5, v64, v59 offset0:8 offset1:10
	v_lshlrev_b32_e32 v56, 16, v46
	v_mul_f32_e32 v57, v3, v57
	v_lshlrev_b32_e32 v58, 16, v49
	v_lshlrev_b32_e32 v59, 16, v50
	v_and_b32_e32 v46, 0xffff0000, v46
	v_mul_f32_e32 v48, v2, v48
	v_and_b32_e32 v49, 0xffff0000, v49
	v_and_b32_e32 v50, 0xffff0000, v50
	v_mul_f32_e32 v65, v3, v65
	v_rndne_f32_e32 v66, v66
	v_mul_f32_e32 v67, v3, v67
	v_mul_f32_e32 v68, v3, v68
	v_mul_f32_e32 v56, v3, v56
	v_rndne_f32_e32 v57, v57
	v_mul_f32_e32 v58, v3, v58
	v_mul_f32_e32 v59, v3, v59
	v_mul_f32_e32 v46, v2, v46
	v_rndne_f32_e32 v48, v48
	v_mul_f32_e32 v49, v2, v49
	v_mul_f32_e32 v50, v2, v50
	v_rndne_f32_e32 v65, v65
	v_cvt_i32_f32_e32 v66, v66
	v_rndne_f32_e32 v67, v67
	v_rndne_f32_e32 v68, v68
	v_rndne_f32_e32 v56, v56
	v_cvt_i32_f32_e32 v57, v57
	v_rndne_f32_e32 v58, v58
	v_rndne_f32_e32 v59, v59
	v_rndne_f32_e32 v46, v46
	v_cvt_i32_f32_e32 v48, v48
	v_rndne_f32_e32 v49, v49
	v_rndne_f32_e32 v50, v50
	v_cvt_i32_f32_e32 v65, v65
	v_cvt_i32_f32_sdwa v67, v67 dst_sel:WORD_1 dst_unused:UNUSED_PAD src0_sel:DWORD
	v_cvt_i32_f32_e32 v68, v68
	v_cvt_i32_f32_e32 v56, v56
	v_cvt_i32_f32_sdwa v58, v58 dst_sel:WORD_1 dst_unused:UNUSED_PAD src0_sel:DWORD
	v_cvt_i32_f32_e32 v59, v59
	v_cvt_i32_f32_e32 v46, v46
	v_cvt_i32_f32_sdwa v49, v49 dst_sel:WORD_1 dst_unused:UNUSED_PAD src0_sel:DWORD
	v_cvt_i32_f32_e32 v50, v50
	v_lshlrev_b32_e32 v66, 8, v66
	v_lshlrev_b32_e32 v57, 8, v57
	v_lshlrev_b32_e32 v48, 8, v48
	v_and_b32_e32 v66, 0xff00, v66
	v_and_b32_e32 v67, 0xff0000, v67
	v_perm_b32 v65, v68, v65, s65
	v_and_b32_e32 v57, 0xff00, v57
	v_and_b32_e32 v58, 0xff0000, v58
	v_perm_b32 v56, v59, v56, s65
	v_and_b32_e32 v48, 0xff00, v48
	v_and_b32_e32 v49, 0xff0000, v49
	v_perm_b32 v46, v50, v46, s65
	v_or3_b32 v65, v65, v66, v67
	v_or3_b32 v56, v56, v57, v58
	v_or3_b32 v46, v46, v48, v49
	v_lshlrev_b32_e32 v49, 16, v52
	ds_write2st64_b32 v99, v65, v56 offset0:52 offset1:54
	v_lshlrev_b32_e32 v48, 16, v51
	v_mul_f32_e32 v49, v8, v49
	v_lshlrev_b32_e32 v50, 16, v53
	v_lshlrev_b32_e32 v56, 16, v55
	v_mul_f32_e32 v48, v8, v48
	v_rndne_f32_e32 v49, v49
	v_mul_f32_e32 v50, v8, v50
	v_mul_f32_e32 v56, v8, v56
	v_rndne_f32_e32 v48, v48
	v_cvt_i32_f32_e32 v49, v49
	v_rndne_f32_e32 v50, v50
	v_rndne_f32_e32 v56, v56
	v_cvt_i32_f32_e32 v48, v48
	v_cvt_i32_f32_sdwa v50, v50 dst_sel:WORD_1 dst_unused:UNUSED_PAD src0_sel:DWORD
	v_cvt_i32_f32_e32 v56, v56
	v_lshlrev_b32_e32 v49, 8, v49
	v_and_b32_e32 v49, 0xff00, v49
	v_and_b32_e32 v50, 0xff0000, v50
	v_perm_b32 v48, v56, v48, s65
	v_or3_b32 v48, v48, v49, v50
	v_and_b32_e32 v50, 0xffff0000, v52
	v_and_b32_e32 v49, 0xffff0000, v51
	v_mul_f32_e32 v50, v4, v50
	v_and_b32_e32 v51, 0xffff0000, v53
	v_and_b32_e32 v52, 0xffff0000, v55
	v_mul_f32_e32 v49, v4, v49
	v_rndne_f32_e32 v50, v50
	v_mul_f32_e32 v51, v4, v51
	v_mul_f32_e32 v52, v4, v52
	v_rndne_f32_e32 v49, v49
	v_cvt_i32_f32_e32 v50, v50
	v_rndne_f32_e32 v51, v51
	v_rndne_f32_e32 v52, v52
	v_cvt_i32_f32_e32 v49, v49
	v_cvt_i32_f32_sdwa v51, v51 dst_sel:WORD_1 dst_unused:UNUSED_PAD src0_sel:DWORD
	v_cvt_i32_f32_e32 v52, v52
	v_lshlrev_b32_e32 v50, 8, v50
	v_and_b32_e32 v50, 0xff00, v50
	v_and_b32_e32 v51, 0xff0000, v51
	v_perm_b32 v49, v52, v49, s65
	v_or3_b32 v49, v49, v50, v51
	v_lshlrev_b32_e32 v50, 16, v44
	v_and_b32_e32 v44, 0xffff0000, v44
	ds_write2st64_b32 v95, v54, v49 offset0:32 offset1:34
	v_lshlrev_b32_e32 v49, 16, v43
	v_lshlrev_b32_e32 v51, 16, v45
	v_lshlrev_b32_e32 v52, 16, v47
	v_and_b32_e32 v43, 0xffff0000, v43
	v_mul_f32_e32 v44, v2, v44
	v_and_b32_e32 v45, 0xffff0000, v45
	v_and_b32_e32 v47, 0xffff0000, v47
	v_mul_f32_e32 v43, v2, v43
	v_rndne_f32_e32 v44, v44
	v_mul_f32_e32 v45, v2, v45
	v_mul_f32_e32 v47, v2, v47
	v_rndne_f32_e32 v43, v43
	v_cvt_i32_f32_e32 v44, v44
	v_rndne_f32_e32 v45, v45
	v_rndne_f32_e32 v47, v47
	v_cvt_i32_f32_e32 v43, v43
	v_cvt_i32_f32_sdwa v45, v45 dst_sel:WORD_1 dst_unused:UNUSED_PAD src0_sel:DWORD
	v_cvt_i32_f32_e32 v47, v47
	v_lshlrev_b32_e32 v44, 8, v44
	v_and_b32_e32 v44, 0xff00, v44
	v_and_b32_e32 v45, 0xff0000, v45
	v_perm_b32 v43, v47, v43, s65
	v_or3_b32 v43, v43, v44, v45
	v_lshlrev_b32_e32 v44, 16, v40
	v_and_b32_e32 v40, 0xffff0000, v40
	ds_write2st64_b32 v75, v46, v43 offset0:76 offset1:78
	v_lshlrev_b32_e32 v43, 16, v39
	v_mul_f32_e32 v44, v8, v44
	v_lshlrev_b32_e32 v45, 16, v41
	v_lshlrev_b32_e32 v46, 16, v42
	v_and_b32_e32 v39, 0xffff0000, v39
	v_mul_f32_e32 v40, v4, v40
	v_and_b32_e32 v41, 0xffff0000, v41
	v_and_b32_e32 v42, 0xffff0000, v42
	v_mul_f32_e32 v43, v8, v43
	v_rndne_f32_e32 v44, v44
	v_mul_f32_e32 v45, v8, v45
	v_mul_f32_e32 v46, v8, v46
	v_mul_f32_e32 v39, v4, v39
	v_rndne_f32_e32 v40, v40
	v_mul_f32_e32 v41, v4, v41
	v_mul_f32_e32 v42, v4, v42
	v_rndne_f32_e32 v43, v43
	v_cvt_i32_f32_e32 v44, v44
	v_rndne_f32_e32 v45, v45
	v_rndne_f32_e32 v46, v46
	v_rndne_f32_e32 v39, v39
	v_cvt_i32_f32_e32 v40, v40
	v_rndne_f32_e32 v41, v41
	v_rndne_f32_e32 v42, v42
	v_cvt_i32_f32_e32 v43, v43
	v_cvt_i32_f32_sdwa v45, v45 dst_sel:WORD_1 dst_unused:UNUSED_PAD src0_sel:DWORD
	v_cvt_i32_f32_e32 v46, v46
	v_cvt_i32_f32_e32 v39, v39
	v_cvt_i32_f32_sdwa v41, v41 dst_sel:WORD_1 dst_unused:UNUSED_PAD src0_sel:DWORD
	v_cvt_i32_f32_e32 v42, v42
	v_lshlrev_b32_e32 v44, 8, v44
	v_lshlrev_b32_e32 v40, 8, v40
	v_and_b32_e32 v44, 0xff00, v44
	v_and_b32_e32 v45, 0xff0000, v45
	v_perm_b32 v43, v46, v43, s65
	v_and_b32_e32 v40, 0xff00, v40
	v_and_b32_e32 v41, 0xff0000, v41
	v_perm_b32 v39, v42, v39, s65
	v_or3_b32 v43, v43, v44, v45
	v_or3_b32 v39, v39, v40, v41
	v_lshlrev_b32_e32 v41, 16, v32
	v_and_b32_e32 v32, 0xffff0000, v32
	v_mul_f32_e32 v50, v3, v50
	ds_write2st64_b32 v5, v48, v43 offset0:12 offset1:14
	v_lshlrev_b32_e32 v40, 16, v31
	v_mul_f32_e32 v41, v3, v41
	v_lshlrev_b32_e32 v42, 16, v33
	v_lshlrev_b32_e32 v43, 16, v34
	v_and_b32_e32 v31, 0xffff0000, v31
	v_mul_f32_e32 v32, v2, v32
	v_and_b32_e32 v33, 0xffff0000, v33
	v_and_b32_e32 v34, 0xffff0000, v34
	v_mul_f32_e32 v49, v3, v49
	v_rndne_f32_e32 v50, v50
	v_mul_f32_e32 v51, v3, v51
	v_mul_f32_e32 v52, v3, v52
	v_mul_f32_e32 v40, v3, v40
	v_rndne_f32_e32 v41, v41
	v_mul_f32_e32 v42, v3, v42
	v_mul_f32_e32 v43, v3, v43
	v_mul_f32_e32 v31, v2, v31
	v_rndne_f32_e32 v32, v32
	v_mul_f32_e32 v33, v2, v33
	v_mul_f32_e32 v34, v2, v34
	v_rndne_f32_e32 v49, v49
	v_cvt_i32_f32_e32 v50, v50
	v_rndne_f32_e32 v51, v51
	v_rndne_f32_e32 v52, v52
	v_rndne_f32_e32 v40, v40
	v_cvt_i32_f32_e32 v41, v41
	v_rndne_f32_e32 v42, v42
	v_rndne_f32_e32 v43, v43
	v_rndne_f32_e32 v31, v31
	v_cvt_i32_f32_e32 v32, v32
	v_rndne_f32_e32 v33, v33
	v_rndne_f32_e32 v34, v34
	v_cvt_i32_f32_e32 v49, v49
	v_cvt_i32_f32_sdwa v51, v51 dst_sel:WORD_1 dst_unused:UNUSED_PAD src0_sel:DWORD
	v_cvt_i32_f32_e32 v52, v52
	v_cvt_i32_f32_e32 v40, v40
	v_cvt_i32_f32_sdwa v42, v42 dst_sel:WORD_1 dst_unused:UNUSED_PAD src0_sel:DWORD
	v_cvt_i32_f32_e32 v43, v43
	v_cvt_i32_f32_e32 v31, v31
	v_cvt_i32_f32_sdwa v33, v33 dst_sel:WORD_1 dst_unused:UNUSED_PAD src0_sel:DWORD
	v_cvt_i32_f32_e32 v34, v34
	v_lshlrev_b32_e32 v50, 8, v50
	v_lshlrev_b32_e32 v41, 8, v41
	v_lshlrev_b32_e32 v32, 8, v32
	v_and_b32_e32 v50, 0xff00, v50
	v_and_b32_e32 v51, 0xff0000, v51
	v_perm_b32 v49, v52, v49, s65
	v_and_b32_e32 v41, 0xff00, v41
	v_and_b32_e32 v42, 0xff0000, v42
	v_perm_b32 v40, v43, v40, s65
	v_and_b32_e32 v32, 0xff00, v32
	v_and_b32_e32 v33, 0xff0000, v33
	v_perm_b32 v31, v34, v31, s65
	v_or3_b32 v49, v49, v50, v51
	v_or3_b32 v40, v40, v41, v42
	v_or3_b32 v31, v31, v32, v33
	v_lshlrev_b32_e32 v33, 16, v36
	ds_write2st64_b32 v99, v49, v40 offset0:56 offset1:58
	v_lshlrev_b32_e32 v32, 16, v35
	v_mul_f32_e32 v33, v8, v33
	v_lshlrev_b32_e32 v34, 16, v37
	v_lshlrev_b32_e32 v40, 16, v38
	v_mul_f32_e32 v32, v8, v32
	v_rndne_f32_e32 v33, v33
	v_mul_f32_e32 v34, v8, v34
	v_mul_f32_e32 v40, v8, v40
	v_rndne_f32_e32 v32, v32
	v_cvt_i32_f32_e32 v33, v33
	v_rndne_f32_e32 v34, v34
	v_rndne_f32_e32 v40, v40
	v_cvt_i32_f32_e32 v32, v32
	v_cvt_i32_f32_sdwa v34, v34 dst_sel:WORD_1 dst_unused:UNUSED_PAD src0_sel:DWORD
	v_cvt_i32_f32_e32 v40, v40
	v_lshlrev_b32_e32 v33, 8, v33
	v_and_b32_e32 v33, 0xff00, v33
	v_and_b32_e32 v34, 0xff0000, v34
	v_perm_b32 v32, v40, v32, s65
	v_or3_b32 v32, v32, v33, v34
	v_and_b32_e32 v34, 0xffff0000, v36
	v_and_b32_e32 v33, 0xffff0000, v35
	v_mul_f32_e32 v34, v4, v34
	v_and_b32_e32 v35, 0xffff0000, v37
	v_and_b32_e32 v36, 0xffff0000, v38
	v_mul_f32_e32 v33, v4, v33
	v_rndne_f32_e32 v34, v34
	v_mul_f32_e32 v35, v4, v35
	v_mul_f32_e32 v36, v4, v36
	v_rndne_f32_e32 v33, v33
	v_cvt_i32_f32_e32 v34, v34
	v_rndne_f32_e32 v35, v35
	v_rndne_f32_e32 v36, v36
	v_cvt_i32_f32_e32 v33, v33
	v_cvt_i32_f32_sdwa v35, v35 dst_sel:WORD_1 dst_unused:UNUSED_PAD src0_sel:DWORD
	v_cvt_i32_f32_e32 v36, v36
	v_lshlrev_b32_e32 v34, 8, v34
	v_and_b32_e32 v34, 0xff00, v34
	v_and_b32_e32 v35, 0xff0000, v35
	v_perm_b32 v33, v36, v33, s65
	v_or3_b32 v33, v33, v34, v35
	v_lshlrev_b32_e32 v34, 16, v28
	v_and_b32_e32 v28, 0xffff0000, v28
	ds_write2st64_b32 v95, v39, v33 offset0:36 offset1:38
	v_lshlrev_b32_e32 v33, 16, v27
	v_lshlrev_b32_e32 v35, 16, v29
	v_lshlrev_b32_e32 v36, 16, v30
	v_and_b32_e32 v27, 0xffff0000, v27
	v_mul_f32_e32 v28, v2, v28
	v_and_b32_e32 v29, 0xffff0000, v29
	v_and_b32_e32 v30, 0xffff0000, v30
	v_mul_f32_e32 v27, v2, v27
	v_rndne_f32_e32 v28, v28
	v_mul_f32_e32 v29, v2, v29
	v_mul_f32_e32 v30, v2, v30
	v_rndne_f32_e32 v27, v27
	v_cvt_i32_f32_e32 v28, v28
	v_rndne_f32_e32 v29, v29
	v_rndne_f32_e32 v30, v30
	v_cvt_i32_f32_e32 v27, v27
	v_cvt_i32_f32_sdwa v29, v29 dst_sel:WORD_1 dst_unused:UNUSED_PAD src0_sel:DWORD
	v_cvt_i32_f32_e32 v30, v30
	v_lshlrev_b32_e32 v28, 8, v28
	v_and_b32_e32 v28, 0xff00, v28
	v_and_b32_e32 v29, 0xff0000, v29
	v_perm_b32 v27, v30, v27, s65
	v_or3_b32 v27, v27, v28, v29
	v_lshlrev_b32_e32 v28, 16, v24
	v_and_b32_e32 v24, 0xffff0000, v24
	ds_write2st64_b32 v75, v31, v27 offset0:80 offset1:82
	v_lshlrev_b32_e32 v27, 16, v23
	v_mul_f32_e32 v28, v8, v28
	v_lshlrev_b32_e32 v29, 16, v25
	v_lshlrev_b32_e32 v30, 16, v26
	v_and_b32_e32 v23, 0xffff0000, v23
	v_mul_f32_e32 v24, v4, v24
	v_and_b32_e32 v25, 0xffff0000, v25
	v_and_b32_e32 v26, 0xffff0000, v26
	v_mul_f32_e32 v27, v8, v27
	v_rndne_f32_e32 v28, v28
	v_mul_f32_e32 v29, v8, v29
	v_mul_f32_e32 v30, v8, v30
	v_mul_f32_e32 v23, v4, v23
	v_rndne_f32_e32 v24, v24
	v_mul_f32_e32 v25, v4, v25
	v_mul_f32_e32 v26, v4, v26
	v_rndne_f32_e32 v27, v27
	v_cvt_i32_f32_e32 v28, v28
	v_rndne_f32_e32 v29, v29
	v_rndne_f32_e32 v30, v30
	v_rndne_f32_e32 v23, v23
	v_cvt_i32_f32_e32 v24, v24
	v_rndne_f32_e32 v25, v25
	v_rndne_f32_e32 v26, v26
	v_cvt_i32_f32_e32 v27, v27
	v_cvt_i32_f32_sdwa v29, v29 dst_sel:WORD_1 dst_unused:UNUSED_PAD src0_sel:DWORD
	v_cvt_i32_f32_e32 v30, v30
	v_cvt_i32_f32_e32 v23, v23
	v_cvt_i32_f32_sdwa v25, v25 dst_sel:WORD_1 dst_unused:UNUSED_PAD src0_sel:DWORD
	v_cvt_i32_f32_e32 v26, v26
	v_lshlrev_b32_e32 v28, 8, v28
	v_lshlrev_b32_e32 v24, 8, v24
	v_and_b32_e32 v28, 0xff00, v28
	v_and_b32_e32 v29, 0xff0000, v29
	v_perm_b32 v27, v30, v27, s65
	v_and_b32_e32 v24, 0xff00, v24
	v_and_b32_e32 v25, 0xff0000, v25
	v_perm_b32 v23, v26, v23, s65
	v_or3_b32 v27, v27, v28, v29
	v_or3_b32 v23, v23, v24, v25
	v_lshlrev_b32_e32 v25, 16, v20
	v_and_b32_e32 v20, 0xffff0000, v20
	v_mul_f32_e32 v34, v3, v34
	ds_write2st64_b32 v5, v32, v27 offset0:16 offset1:18
	v_lshlrev_b32_e32 v24, 16, v19
	v_mul_f32_e32 v25, v3, v25
	v_lshlrev_b32_e32 v26, 16, v21
	v_lshlrev_b32_e32 v27, 16, v22
	v_and_b32_e32 v19, 0xffff0000, v19
	v_mul_f32_e32 v20, v2, v20
	v_and_b32_e32 v21, 0xffff0000, v21
	v_and_b32_e32 v22, 0xffff0000, v22
	v_mul_f32_e32 v33, v3, v33
	v_rndne_f32_e32 v34, v34
	v_mul_f32_e32 v35, v3, v35
	v_mul_f32_e32 v36, v3, v36
	v_mul_f32_e32 v24, v3, v24
	v_rndne_f32_e32 v25, v25
	v_mul_f32_e32 v26, v3, v26
	v_mul_f32_e32 v27, v3, v27
	v_mul_f32_e32 v19, v2, v19
	v_rndne_f32_e32 v20, v20
	v_mul_f32_e32 v21, v2, v21
	v_mul_f32_e32 v22, v2, v22
	v_rndne_f32_e32 v33, v33
	v_cvt_i32_f32_e32 v34, v34
	v_rndne_f32_e32 v35, v35
	v_rndne_f32_e32 v36, v36
	v_rndne_f32_e32 v24, v24
	v_cvt_i32_f32_e32 v25, v25
	v_rndne_f32_e32 v26, v26
	v_rndne_f32_e32 v27, v27
	v_rndne_f32_e32 v19, v19
	v_cvt_i32_f32_e32 v20, v20
	v_rndne_f32_e32 v21, v21
	v_rndne_f32_e32 v22, v22
	v_cvt_i32_f32_e32 v33, v33
	v_cvt_i32_f32_sdwa v35, v35 dst_sel:WORD_1 dst_unused:UNUSED_PAD src0_sel:DWORD
	v_cvt_i32_f32_e32 v36, v36
	v_cvt_i32_f32_e32 v24, v24
	v_cvt_i32_f32_sdwa v26, v26 dst_sel:WORD_1 dst_unused:UNUSED_PAD src0_sel:DWORD
	v_cvt_i32_f32_e32 v27, v27
	v_cvt_i32_f32_e32 v19, v19
	v_cvt_i32_f32_sdwa v21, v21 dst_sel:WORD_1 dst_unused:UNUSED_PAD src0_sel:DWORD
	v_cvt_i32_f32_e32 v22, v22
	v_lshlrev_b32_e32 v34, 8, v34
	v_lshlrev_b32_e32 v25, 8, v25
	v_lshlrev_b32_e32 v20, 8, v20
	v_and_b32_e32 v34, 0xff00, v34
	v_and_b32_e32 v35, 0xff0000, v35
	v_perm_b32 v33, v36, v33, s65
	v_and_b32_e32 v25, 0xff00, v25
	v_and_b32_e32 v26, 0xff0000, v26
	v_perm_b32 v24, v27, v24, s65
	v_and_b32_e32 v20, 0xff00, v20
	v_and_b32_e32 v21, 0xff0000, v21
	v_perm_b32 v19, v22, v19, s65
	v_or3_b32 v33, v33, v34, v35
	v_or3_b32 v24, v24, v25, v26
	v_or3_b32 v19, v19, v20, v21
	v_lshlrev_b32_e32 v21, 16, v16
	ds_write2st64_b32 v99, v33, v24 offset0:60 offset1:62
	v_lshlrev_b32_e32 v20, 16, v15
	v_mul_f32_e32 v21, v8, v21
	v_lshlrev_b32_e32 v22, 16, v17
	v_lshlrev_b32_e32 v24, 16, v18
	v_mul_f32_e32 v20, v8, v20
	v_rndne_f32_e32 v21, v21
	v_mul_f32_e32 v22, v8, v22
	v_mul_f32_e32 v8, v8, v24
	v_rndne_f32_e32 v20, v20
	v_cvt_i32_f32_e32 v21, v21
	v_rndne_f32_e32 v22, v22
	v_rndne_f32_e32 v8, v8
	v_cvt_i32_f32_e32 v20, v20
	v_cvt_i32_f32_sdwa v22, v22 dst_sel:WORD_1 dst_unused:UNUSED_PAD src0_sel:DWORD
	v_cvt_i32_f32_e32 v8, v8
	v_lshlrev_b32_e32 v21, 8, v21
	v_and_b32_e32 v21, 0xff00, v21
	v_and_b32_e32 v22, 0xff0000, v22
	v_perm_b32 v8, v8, v20, s65
	v_or3_b32 v8, v8, v21, v22
	v_add_u32_e32 v20, 0x1400, v5
	ds_write2_b32 v20, v8, v9 offset1:132
	v_and_b32_e32 v9, 0xffff0000, v16
	v_and_b32_e32 v8, 0xffff0000, v15
	v_mul_f32_e32 v9, v4, v9
	v_and_b32_e32 v15, 0xffff0000, v17
	v_and_b32_e32 v16, 0xffff0000, v18
	v_mul_f32_e32 v8, v4, v8
	v_rndne_f32_e32 v9, v9
	v_mul_f32_e32 v15, v4, v15
	v_mul_f32_e32 v4, v4, v16
	v_rndne_f32_e32 v8, v8
	v_cvt_i32_f32_e32 v9, v9
	v_rndne_f32_e32 v15, v15
	v_rndne_f32_e32 v4, v4
	v_cvt_i32_f32_e32 v8, v8
	v_cvt_i32_f32_sdwa v15, v15 dst_sel:WORD_1 dst_unused:UNUSED_PAD src0_sel:DWORD
	v_cvt_i32_f32_e32 v4, v4
	v_lshlrev_b32_e32 v9, 8, v9
	v_and_b32_e32 v9, 0xff00, v9
	v_and_b32_e32 v15, 0xff0000, v15
	v_perm_b32 v4, v4, v8, s65
	v_or3_b32 v4, v4, v9, v15
	v_lshlrev_b32_e32 v8, 16, v10
	ds_write2st64_b32 v95, v23, v4 offset0:40 offset1:42
	v_lshlrev_b32_e32 v4, 16, v7
	v_mul_f32_e32 v8, v3, v8
	v_lshlrev_b32_e32 v9, 16, v13
	v_lshlrev_b32_e32 v15, 16, v14
	v_mul_f32_e32 v4, v3, v4
	v_rndne_f32_e32 v8, v8
	v_mul_f32_e32 v9, v3, v9
	v_mul_f32_e32 v3, v3, v15
	v_rndne_f32_e32 v4, v4
	v_cvt_i32_f32_e32 v8, v8
	v_rndne_f32_e32 v9, v9
	v_rndne_f32_e32 v3, v3
	v_cvt_i32_f32_e32 v4, v4
	v_cvt_i32_f32_sdwa v9, v9 dst_sel:WORD_1 dst_unused:UNUSED_PAD src0_sel:DWORD
	v_cvt_i32_f32_e32 v3, v3
	v_lshlrev_b32_e32 v8, 8, v8
	v_and_b32_e32 v8, 0xff00, v8
	v_and_b32_e32 v9, 0xff0000, v9
	v_perm_b32 v3, v3, v4, s65
	v_or3_b32 v3, v3, v8, v9
	v_add_u32_e32 v4, 0x4000, v5
	ds_write2_b32 v4, v3, v6 offset0:8 offset1:140
	v_and_b32_e32 v4, 0xffff0000, v10
	v_and_b32_e32 v3, 0xffff0000, v7
	v_mul_f32_e32 v4, v2, v4
	v_and_b32_e32 v5, 0xffff0000, v13
	v_and_b32_e32 v6, 0xffff0000, v14
	v_mul_f32_e32 v3, v2, v3
	v_rndne_f32_e32 v4, v4
	v_mul_f32_e32 v5, v2, v5
	v_mul_f32_e32 v2, v2, v6
	v_rndne_f32_e32 v3, v3
	v_cvt_i32_f32_e32 v4, v4
	v_rndne_f32_e32 v5, v5
	v_rndne_f32_e32 v2, v2
	v_cvt_i32_f32_e32 v3, v3
	v_cvt_i32_f32_sdwa v5, v5 dst_sel:WORD_1 dst_unused:UNUSED_PAD src0_sel:DWORD
	v_cvt_i32_f32_e32 v2, v2
	v_lshlrev_b32_e32 v4, 8, v4
	v_and_b32_e32 v4, 0xff00, v4
	v_and_b32_e32 v5, 0xff0000, v5
	v_perm_b32 v2, v2, v3, s65
	v_or3_b32 v2, v2, v4, v5
	ds_write2st64_b32 v75, v19, v2 offset0:84 offset1:86
	s_waitcnt lgkmcnt(0)
	s_barrier
	v_cmp_eq_u32_e32 vcc, 0, v0
	s_and_saveexec_b64 s[98:99], vcc
	v_mov_b32_e32 v200, 1
	s_nop 0
	global_atomic_add v200, v11, v200, s[16:17] sc0
	s_mov_b64 exec, s[98:99]
	v_cmp_gt_i32_e32 vcc, s69, v12
	s_and_saveexec_b64 s[4:5], vcc
	s_cbranch_execz .LBB0_252
	v_lshlrev_b32_e32 v2, 4, v12
	s_mov_b64 s[8:9], 0
